# prep: transpose tiles take the block IDs right after the gate blocks (empty blocks last) + all slow x-row loads of the gate blocks issued up front
# speedup vs baseline: 1.0055x; 1.0055x over previous
_Z11prep_kernelPKfS0_S0_S0_S0_S0_S0_S0_S0_S0_S0_S0_PtS1_S1_S1_S1_S1_:
	s_load_dwordx2 s[20:21], s[0:1], 0x0
	s_add_i32 s3, s2, 0xfffffa00
	s_cmpk_gt_u32 s3, 0x3ff
	s_mov_b64 s[4:5], -1
	s_cbranch_scc1 .LBB13_3
	s_andn2_b64 vcc, exec, s[4:5]
	s_cbranch_vccz .LBB13_18

.LBB13_3:
	s_cmpk_lt_i32 s2, 0x100
	v_lshrrev_b32_e32 v1, 6, v0
	v_and_b32_e32 v36, 63, v0
	s_cbranch_scc0 .LBB13_5
	v_bfe_u32 v13, v0, 4, 2
	v_and_b32_e32 v12, 15, v0
	s_lshl_b32 s22, s2, 4
	v_lshlrev_b32_e32 v2, 3, v13
	v_lshl_or_b32 v14, v1, 8, v2
	v_or_b32_e32 v2, s22, v12
	s_load_dwordx8 s[4:11], s[0:1], 0x30
	s_load_dwordx2 s[26:27], s[0:1], 0x60
	v_ashrrev_i32_e32 v3, 31, v2
	v_lshlrev_b64 v[2:3], 12, v[2:3]
	s_waitcnt lgkmcnt(0)
	v_lshl_add_u64 v[2:3], s[20:21], 0, v[2:3]
	v_lshlrev_b32_e32 v18, 2, v14
	v_mov_b32_e32 v19, 0
	v_lshl_or_b32 v14, v14, 4, v12
	v_lshl_add_u64 v[10:11], v[2:3], 0, v[18:19]
	v_subrev_u32_e32 v108, s20, v10
	v_lshrrev_b32_e32 v108, 1, v108
	global_load_dwordx4 v[116:119], v[10:11], off offset:528
	global_load_dwordx4 v[112:115], v[10:11], off offset:512
	global_load_dwordx4 v[124:127], v[10:11], off offset:656
	global_load_dwordx4 v[120:123], v[10:11], off offset:640
	global_load_dwordx4 v[132:135], v[10:11], off offset:784
	global_load_dwordx4 v[128:131], v[10:11], off offset:768
	global_load_dwordx4 v[140:143], v[10:11], off offset:912
	global_load_dwordx4 v[136:139], v[10:11], off offset:896
	global_load_dwordx4 v[148:151], v[10:11], off offset:400
	global_load_dwordx4 v[144:147], v[10:11], off offset:384
	v_or_b32_e32 v18, 0x200, v14
	v_lshlrev_b64 v[16:17], 2, v[18:19]
	v_lshlrev_b32_e32 v15, 2, v14
	v_lshl_add_u64 v[28:29], s[4:5], 0, v[16:17]
	v_lshl_add_u64 v[16:17], s[10:11], 0, v[16:17]
	v_or_b32_e32 v18, 0x400, v14
	global_load_dwordx4 v[2:5], v[10:11], off offset:16
	global_load_dwordx4 v[6:9], v[10:11], off
	global_load_dword v37, v15, s[4:5]
	global_load_dword v48, v15, s[10:11]
	global_load_dword v49, v15, s[4:5] offset:64
	global_load_dword v50, v15, s[10:11] offset:64
	global_load_dword v51, v15, s[4:5] offset:128
	global_load_dword v52, v15, s[10:11] offset:128
	global_load_dword v53, v15, s[4:5] offset:192
	global_load_dword v54, v15, s[10:11] offset:192
	global_load_dword v55, v15, s[4:5] offset:256
	global_load_dword v56, v15, s[10:11] offset:256
	global_load_dword v57, v15, s[4:5] offset:320
	global_load_dword v58, v15, s[10:11] offset:320
	global_load_dword v59, v15, s[4:5] offset:384
	global_load_dword v60, v15, s[10:11] offset:384
	global_load_dword v61, v15, s[4:5] offset:448
	global_load_dword v62, v15, s[10:11] offset:448
	global_load_dwordx4 v[20:23], v[10:11], off offset:144
	global_load_dwordx4 v[24:27], v[10:11], off offset:128
	global_load_dword v63, v[28:29], off
	global_load_dword v64, v[16:17], off
	global_load_dword v65, v15, s[4:5] offset:2112
	global_load_dword v66, v15, s[10:11] offset:2112
	global_load_dword v67, v15, s[4:5] offset:2176
	global_load_dword v68, v15, s[10:11] offset:2176
	global_load_dword v69, v15, s[4:5] offset:2240
	global_load_dword v70, v15, s[10:11] offset:2240
	global_load_dword v71, v15, s[4:5] offset:2304
	global_load_dword v72, v15, s[10:11] offset:2304
	global_load_dword v73, v15, s[4:5] offset:2368
	global_load_dword v74, v15, s[10:11] offset:2368
	global_load_dword v75, v15, s[4:5] offset:2432
	global_load_dword v76, v15, s[10:11] offset:2432
	global_load_dword v77, v15, s[4:5] offset:2496
	global_load_dword v78, v15, s[10:11] offset:2496
	s_nop 0
	global_load_dwordx4 v[28:31], v[10:11], off offset:272
	global_load_dwordx4 v[32:35], v[10:11], off offset:256
	v_lshlrev_b64 v[16:17], 2, v[18:19]
	v_lshl_add_u64 v[38:39], s[4:5], 0, v[16:17]
	v_lshl_add_u64 v[16:17], s[10:11], 0, v[16:17]
	v_or_b32_e32 v18, 0x410, v14
	global_load_dword v79, v[16:17], off
	v_lshlrev_b64 v[16:17], 2, v[18:19]
	global_load_dword v15, v[38:39], off
	v_lshl_add_u64 v[38:39], s[4:5], 0, v[16:17]
	v_lshl_add_u64 v[16:17], s[10:11], 0, v[16:17]
	v_or_b32_e32 v18, 0x420, v14
	global_load_dword v81, v[16:17], off
	v_lshlrev_b64 v[16:17], 2, v[18:19]
	global_load_dword v80, v[38:39], off
	v_lshl_add_u64 v[38:39], s[4:5], 0, v[16:17]
	v_lshl_add_u64 v[16:17], s[10:11], 0, v[16:17]
	v_or_b32_e32 v18, 0x430, v14
	global_load_dword v83, v[16:17], off
	v_lshlrev_b64 v[16:17], 2, v[18:19]
	global_load_dword v82, v[38:39], off
	v_lshl_add_u64 v[38:39], s[4:5], 0, v[16:17]
	v_lshl_add_u64 v[16:17], s[10:11], 0, v[16:17]
	v_or_b32_e32 v18, 0x440, v14
	global_load_dword v85, v[16:17], off
	v_lshlrev_b64 v[16:17], 2, v[18:19]
	global_load_dword v84, v[38:39], off
	v_lshl_add_u64 v[38:39], s[4:5], 0, v[16:17]
	v_lshl_add_u64 v[16:17], s[10:11], 0, v[16:17]
	v_or_b32_e32 v18, 0x450, v14
	global_load_dword v87, v[16:17], off
	v_lshlrev_b64 v[16:17], 2, v[18:19]
	global_load_dword v86, v[38:39], off
	v_lshl_add_u64 v[38:39], s[4:5], 0, v[16:17]
	v_lshl_add_u64 v[16:17], s[10:11], 0, v[16:17]
	v_or_b32_e32 v18, 0x460, v14
	global_load_dword v89, v[16:17], off
	v_lshlrev_b64 v[16:17], 2, v[18:19]
	global_load_dword v88, v[38:39], off
	v_lshl_add_u64 v[38:39], s[4:5], 0, v[16:17]
	v_lshl_add_u64 v[16:17], s[10:11], 0, v[16:17]
	v_or_b32_e32 v18, 0x470, v14
	global_load_dword v91, v[16:17], off
	v_lshlrev_b64 v[16:17], 2, v[18:19]
	global_load_dword v90, v[38:39], off
	v_lshl_add_u64 v[38:39], s[4:5], 0, v[16:17]
	v_lshl_add_u64 v[16:17], s[10:11], 0, v[16:17]
	v_or_b32_e32 v18, 0x600, v14
	global_load_dword v92, v[38:39], off
	global_load_dword v93, v[16:17], off
	s_nop 0
	v_lshlrev_b64 v[16:17], 2, v[18:19]
	v_lshl_add_u64 v[46:47], s[4:5], 0, v[16:17]
	v_lshl_add_u64 v[16:17], s[10:11], 0, v[16:17]
	v_or_b32_e32 v18, 0x610, v14
	global_load_dword v95, v[16:17], off
	v_lshlrev_b64 v[16:17], 2, v[18:19]
	global_load_dword v94, v[46:47], off
	v_lshl_add_u64 v[46:47], s[4:5], 0, v[16:17]
	v_lshl_add_u64 v[16:17], s[10:11], 0, v[16:17]
	v_or_b32_e32 v18, 0x620, v14
	global_load_dword v97, v[16:17], off
	v_lshlrev_b64 v[16:17], 2, v[18:19]
	global_load_dword v96, v[46:47], off
	v_lshl_add_u64 v[46:47], s[4:5], 0, v[16:17]
	v_lshl_add_u64 v[16:17], s[10:11], 0, v[16:17]
	v_or_b32_e32 v18, 0x630, v14
	global_load_dword v99, v[16:17], off
	v_lshlrev_b64 v[16:17], 2, v[18:19]
	global_load_dword v98, v[46:47], off
	v_lshl_add_u64 v[46:47], s[4:5], 0, v[16:17]
	v_lshl_add_u64 v[16:17], s[10:11], 0, v[16:17]
	v_or_b32_e32 v18, 0x640, v14
	global_load_dword v101, v[16:17], off
	v_lshlrev_b64 v[16:17], 2, v[18:19]
	global_load_dword v100, v[46:47], off
	v_lshl_add_u64 v[46:47], s[4:5], 0, v[16:17]
	v_lshl_add_u64 v[16:17], s[10:11], 0, v[16:17]
	v_or_b32_e32 v18, 0x650, v14
	global_load_dword v103, v[16:17], off
	v_lshlrev_b64 v[16:17], 2, v[18:19]
	global_load_dword v102, v[46:47], off
	v_lshl_add_u64 v[46:47], s[4:5], 0, v[16:17]
	v_lshl_add_u64 v[16:17], s[10:11], 0, v[16:17]
	v_or_b32_e32 v18, 0x660, v14
	global_load_dword v105, v[16:17], off
	v_lshlrev_b64 v[16:17], 2, v[18:19]
	global_load_dword v104, v[46:47], off
	v_lshl_add_u64 v[46:47], s[4:5], 0, v[16:17]
	v_lshl_add_u64 v[16:17], s[10:11], 0, v[16:17]
	v_or_b32_e32 v18, 0x670, v14
	global_load_dword v107, v[16:17], off
	v_lshlrev_b64 v[16:17], 2, v[18:19]
	global_load_dword v106, v[46:47], off
	v_lshl_add_u64 v[46:47], s[4:5], 0, v[16:17]
	v_lshl_add_u64 v[16:17], s[10:11], 0, v[16:17]
	global_load_dword v18, v[46:47], off
	s_mov_b32 s23, 0
	global_load_dword v16, v[16:17], off
	s_load_dwordx2 s[24:25], s[0:1], 0x88
	s_load_dwordx4 s[12:15], s[0:1], 0x78
	s_load_dwordx4 s[16:19], s[0:1], 0x50
	s_waitcnt vmcnt(60)
	v_cvt_pk_f16_f32 v6, v6, v7
	v_cvt_pk_f16_f32 v7, v8, v9
	v_cvt_pk_f16_f32 v8, v2, v3
	v_cvt_pk_f16_f32 v9, v4, v5
	v_cvt_pk_f16_f32 v2, v37, v49
	v_cvt_pk_f16_f32 v3, v51, v53
	s_waitcnt vmcnt(57)
	v_cvt_pk_f16_f32 v4, v55, v57
	s_waitcnt vmcnt(53)
	v_cvt_pk_f16_f32 v5, v59, v61
	v_cvt_pk_f16_f32 v46, v48, v50
	v_cvt_pk_f16_f32 v47, v52, v54
	v_mfma_f32_16x16x32_f16 a[0:3], v[6:9], v[2:5], 0
	global_store_dwordx4 v108, v[6:9], s[26:27] offset:0
	v_cvt_pk_f16_f32 v48, v56, v58
	s_waitcnt vmcnt(53)
	v_cvt_pk_f16_f32 v49, v60, v62
	s_waitcnt vmcnt(51)
	v_cvt_pk_f16_f32 v2, v24, v25
	v_cvt_pk_f16_f32 v3, v26, v27
	v_cvt_pk_f16_f32 v4, v20, v21
	v_cvt_pk_f16_f32 v5, v22, v23
	v_mfma_f32_16x16x32_f16 a[4:7], v[6:9], v[46:49], 0
	s_waitcnt vmcnt(48)
	v_cvt_pk_f16_f32 v6, v63, v65
	s_waitcnt vmcnt(47)
	v_cvt_pk_f16_f32 v20, v64, v66
	s_waitcnt vmcnt(44)
	v_cvt_pk_f16_f32 v7, v67, v69
	s_waitcnt vmcnt(40)
	v_cvt_pk_f16_f32 v8, v71, v73
	s_waitcnt vmcnt(36)
	v_cvt_pk_f16_f32 v9, v75, v77
	v_cvt_pk_f16_f32 v21, v68, v70
	v_cvt_pk_f16_f32 v22, v72, v74
	s_waitcnt vmcnt(35)
	v_cvt_pk_f16_f32 v23, v76, v78
	v_mfma_f32_16x16x32_f16 a[0:3], v[2:5], v[6:9], a[0:3]
	global_store_dwordx4 v108, v[2:5], s[26:27] offset:64
	s_waitcnt vmcnt(30)
	v_cvt_pk_f16_f32 v6, v15, v80
	s_waitcnt vmcnt(26)
	v_cvt_pk_f16_f32 v7, v82, v84
	s_waitcnt vmcnt(22)
	v_cvt_pk_f16_f32 v8, v86, v88
	v_mfma_f32_16x16x32_f16 a[4:7], v[2:5], v[20:23], a[4:7]
	v_cvt_pk_f16_f32 v2, v32, v33
	v_cvt_pk_f16_f32 v3, v34, v35
	v_cvt_pk_f16_f32 v4, v28, v29
	v_cvt_pk_f16_f32 v5, v30, v31
	v_cvt_pk_f16_f32 v20, v79, v81
	s_waitcnt vmcnt(19)
	v_cvt_pk_f16_f32 v9, v90, v92
	v_cvt_pk_f16_f32 v21, v83, v85
	v_cvt_pk_f16_f32 v22, v87, v89
	s_waitcnt vmcnt(18)
	v_cvt_pk_f16_f32 v23, v91, v93
	v_mfma_f32_16x16x32_f16 a[0:3], v[2:5], v[6:9], a[0:3]
	global_store_dwordx4 v108, v[2:5], s[26:27] offset:128
	s_waitcnt vmcnt(15)
	v_cvt_pk_f16_f32 v6, v94, v96
	s_waitcnt vmcnt(11)
	v_cvt_pk_f16_f32 v7, v98, v100
	s_waitcnt vmcnt(7)
	v_cvt_pk_f16_f32 v8, v102, v104
	v_mfma_f32_16x16x32_f16 a[8:11], v[2:5], v[20:23], a[4:7]
	v_cvt_pk_f16_f32 v2, v144, v145
	v_cvt_pk_f16_f32 v3, v146, v147
	v_cvt_pk_f16_f32 v4, v148, v149
	v_cvt_pk_f16_f32 v5, v150, v151
	v_cvt_pk_f16_f32 v20, v95, v97
	s_waitcnt vmcnt(4)
	v_cvt_pk_f16_f32 v9, v106, v18
	v_cvt_pk_f16_f32 v21, v99, v101
	v_cvt_pk_f16_f32 v22, v103, v105
	s_waitcnt vmcnt(3)
	v_cvt_pk_f16_f32 v23, v107, v16
	v_mfma_f32_16x16x32_f16 a[4:7], v[2:5], v[6:9], a[0:3]
	global_store_dwordx4 v108, v[2:5], s[26:27] offset:192
	s_nop 0
	v_mfma_f32_16x16x32_f16 a[0:3], v[2:5], v[20:23], a[8:11]
	v_or_b32_e32 v18, 0x800, v14
	v_lshlrev_b64 v[16:17], 2, v[18:19]
	v_lshl_add_u64 v[20:21], s[4:5], 0, v[16:17]
	v_lshl_add_u64 v[16:17], s[10:11], 0, v[16:17]
	v_or_b32_e32 v18, 0x810, v14
	global_load_dword v46, v[16:17], off
	v_lshlrev_b64 v[16:17], 2, v[18:19]
	global_load_dword v37, v[20:21], off
	v_lshl_add_u64 v[20:21], s[4:5], 0, v[16:17]
	v_lshl_add_u64 v[16:17], s[10:11], 0, v[16:17]
	v_or_b32_e32 v18, 0x820, v14
	global_load_dword v48, v[16:17], off
	v_lshlrev_b64 v[16:17], 2, v[18:19]
	global_load_dword v47, v[20:21], off
	v_lshl_add_u64 v[20:21], s[4:5], 0, v[16:17]
	v_lshl_add_u64 v[16:17], s[10:11], 0, v[16:17]
	v_or_b32_e32 v18, 0x830, v14
	global_load_dword v50, v[16:17], off
	v_lshlrev_b64 v[16:17], 2, v[18:19]
	global_load_dword v49, v[20:21], off
	v_lshl_add_u64 v[20:21], s[4:5], 0, v[16:17]
	v_lshl_add_u64 v[16:17], s[10:11], 0, v[16:17]
	v_or_b32_e32 v18, 0x840, v14
	global_load_dword v52, v[16:17], off
	v_lshlrev_b64 v[16:17], 2, v[18:19]
	global_load_dword v51, v[20:21], off
	v_lshl_add_u64 v[20:21], s[4:5], 0, v[16:17]
	v_lshl_add_u64 v[16:17], s[10:11], 0, v[16:17]
	v_or_b32_e32 v18, 0x850, v14
	global_load_dword v54, v[16:17], off
	v_lshlrev_b64 v[16:17], 2, v[18:19]
	global_load_dword v53, v[20:21], off
	v_lshl_add_u64 v[20:21], s[4:5], 0, v[16:17]
	v_lshl_add_u64 v[16:17], s[10:11], 0, v[16:17]
	v_or_b32_e32 v18, 0x860, v14
	global_load_dword v56, v[16:17], off
	v_lshlrev_b64 v[16:17], 2, v[18:19]
	global_load_dword v55, v[20:21], off
	v_lshl_add_u64 v[20:21], s[4:5], 0, v[16:17]
	v_lshl_add_u64 v[16:17], s[10:11], 0, v[16:17]
	v_or_b32_e32 v18, 0x870, v14
	global_load_dword v58, v[16:17], off
	v_lshlrev_b64 v[16:17], 2, v[18:19]
	global_load_dword v57, v[20:21], off
	v_lshl_add_u64 v[20:21], s[4:5], 0, v[16:17]
	v_lshl_add_u64 v[16:17], s[10:11], 0, v[16:17]
	v_or_b32_e32 v18, 0xa00, v14
	global_load_dword v59, v[20:21], off
	global_load_dword v60, v[16:17], off
	s_nop 0
	v_lshlrev_b64 v[16:17], 2, v[18:19]
	v_lshl_add_u64 v[28:29], s[4:5], 0, v[16:17]
	v_lshl_add_u64 v[16:17], s[10:11], 0, v[16:17]
	v_or_b32_e32 v18, 0xa10, v14
	global_load_dword v62, v[16:17], off
	v_lshlrev_b64 v[16:17], 2, v[18:19]
	global_load_dword v61, v[28:29], off
	v_lshl_add_u64 v[28:29], s[4:5], 0, v[16:17]
	v_lshl_add_u64 v[16:17], s[10:11], 0, v[16:17]
	v_or_b32_e32 v18, 0xa20, v14
	global_load_dword v64, v[16:17], off
	v_lshlrev_b64 v[16:17], 2, v[18:19]
	global_load_dword v63, v[28:29], off
	v_lshl_add_u64 v[28:29], s[4:5], 0, v[16:17]
	v_lshl_add_u64 v[16:17], s[10:11], 0, v[16:17]
	v_or_b32_e32 v18, 0xa30, v14
	global_load_dword v66, v[16:17], off
	v_lshlrev_b64 v[16:17], 2, v[18:19]
	global_load_dword v65, v[28:29], off
	v_lshl_add_u64 v[28:29], s[4:5], 0, v[16:17]
	v_lshl_add_u64 v[16:17], s[10:11], 0, v[16:17]
	v_or_b32_e32 v18, 0xa40, v14
	global_load_dword v68, v[16:17], off
	v_lshlrev_b64 v[16:17], 2, v[18:19]
	global_load_dword v67, v[28:29], off
	v_lshl_add_u64 v[28:29], s[4:5], 0, v[16:17]
	v_lshl_add_u64 v[16:17], s[10:11], 0, v[16:17]
	v_or_b32_e32 v18, 0xa50, v14
	global_load_dword v70, v[16:17], off
	v_lshlrev_b64 v[16:17], 2, v[18:19]
	global_load_dword v69, v[28:29], off
	v_lshl_add_u64 v[28:29], s[4:5], 0, v[16:17]
	v_lshl_add_u64 v[16:17], s[10:11], 0, v[16:17]
	v_or_b32_e32 v18, 0xa60, v14
	global_load_dword v72, v[16:17], off
	v_lshlrev_b64 v[16:17], 2, v[18:19]
	global_load_dword v71, v[28:29], off
	v_lshl_add_u64 v[28:29], s[4:5], 0, v[16:17]
	v_lshl_add_u64 v[16:17], s[10:11], 0, v[16:17]
	v_or_b32_e32 v18, 0xa70, v14
	global_load_dword v74, v[16:17], off
	v_lshlrev_b64 v[16:17], 2, v[18:19]
	global_load_dword v73, v[28:29], off
	v_lshl_add_u64 v[28:29], s[4:5], 0, v[16:17]
	v_lshl_add_u64 v[16:17], s[10:11], 0, v[16:17]
	v_or_b32_e32 v18, 0xc00, v14
	global_load_dword v75, v[28:29], off
	global_load_dword v76, v[16:17], off
	s_nop 0
	v_lshlrev_b64 v[16:17], 2, v[18:19]
	v_lshl_add_u64 v[38:39], s[4:5], 0, v[16:17]
	v_lshl_add_u64 v[16:17], s[10:11], 0, v[16:17]
	v_or_b32_e32 v18, 0xc10, v14
	global_load_dword v78, v[16:17], off
	v_lshlrev_b64 v[16:17], 2, v[18:19]
	global_load_dword v77, v[38:39], off
	v_lshl_add_u64 v[38:39], s[4:5], 0, v[16:17]
	v_lshl_add_u64 v[16:17], s[10:11], 0, v[16:17]
	v_or_b32_e32 v18, 0xc20, v14
	global_load_dword v80, v[16:17], off
	v_lshlrev_b64 v[16:17], 2, v[18:19]
	global_load_dword v79, v[38:39], off
	v_lshl_add_u64 v[38:39], s[4:5], 0, v[16:17]
	v_lshl_add_u64 v[16:17], s[10:11], 0, v[16:17]
	v_or_b32_e32 v18, 0xc30, v14
	global_load_dword v82, v[16:17], off
	v_lshlrev_b64 v[16:17], 2, v[18:19]
	global_load_dword v81, v[38:39], off
	v_lshl_add_u64 v[38:39], s[4:5], 0, v[16:17]
	v_lshl_add_u64 v[16:17], s[10:11], 0, v[16:17]
	v_or_b32_e32 v18, 0xc40, v14
	global_load_dword v84, v[16:17], off
	v_lshlrev_b64 v[16:17], 2, v[18:19]
	global_load_dword v83, v[38:39], off
	v_lshl_add_u64 v[38:39], s[4:5], 0, v[16:17]
	v_lshl_add_u64 v[16:17], s[10:11], 0, v[16:17]
	v_or_b32_e32 v18, 0xc50, v14
	global_load_dword v86, v[16:17], off
	v_lshlrev_b64 v[16:17], 2, v[18:19]
	global_load_dword v85, v[38:39], off
	v_lshl_add_u64 v[38:39], s[4:5], 0, v[16:17]
	v_lshl_add_u64 v[16:17], s[10:11], 0, v[16:17]
	v_or_b32_e32 v18, 0xc60, v14
	global_load_dword v88, v[16:17], off
	v_lshlrev_b64 v[16:17], 2, v[18:19]
	global_load_dword v87, v[38:39], off
	v_lshl_add_u64 v[38:39], s[4:5], 0, v[16:17]
	v_lshl_add_u64 v[16:17], s[10:11], 0, v[16:17]
	v_or_b32_e32 v18, 0xc70, v14
	global_load_dword v90, v[16:17], off
	v_lshlrev_b64 v[16:17], 2, v[18:19]
	global_load_dword v89, v[38:39], off
	v_lshl_add_u64 v[38:39], s[4:5], 0, v[16:17]
	v_lshl_add_u64 v[16:17], s[10:11], 0, v[16:17]
	v_or_b32_e32 v18, 0xe00, v14
	global_load_dword v91, v[38:39], off
	global_load_dword v92, v[16:17], off
	s_nop 0
	v_lshlrev_b64 v[10:11], 2, v[18:19]
	v_lshl_add_u64 v[16:17], s[4:5], 0, v[10:11]
	v_lshl_add_u64 v[10:11], s[10:11], 0, v[10:11]
	v_or_b32_e32 v18, 0xe10, v14
	global_load_dword v94, v[10:11], off
	v_lshlrev_b64 v[10:11], 2, v[18:19]
	global_load_dword v93, v[16:17], off
	v_lshl_add_u64 v[16:17], s[4:5], 0, v[10:11]
	v_lshl_add_u64 v[10:11], s[10:11], 0, v[10:11]
	v_or_b32_e32 v18, 0xe20, v14
	global_load_dword v96, v[10:11], off
	v_lshlrev_b64 v[10:11], 2, v[18:19]
	global_load_dword v95, v[16:17], off
	v_lshl_add_u64 v[16:17], s[4:5], 0, v[10:11]
	v_lshl_add_u64 v[10:11], s[10:11], 0, v[10:11]
	v_or_b32_e32 v18, 0xe30, v14
	global_load_dword v98, v[10:11], off
	v_lshlrev_b64 v[10:11], 2, v[18:19]
	global_load_dword v97, v[16:17], off
	v_lshl_add_u64 v[16:17], s[4:5], 0, v[10:11]
	v_lshl_add_u64 v[10:11], s[10:11], 0, v[10:11]
	v_or_b32_e32 v18, 0xe40, v14
	global_load_dword v100, v[10:11], off
	v_lshlrev_b64 v[10:11], 2, v[18:19]
	global_load_dword v99, v[16:17], off
	v_lshl_add_u64 v[16:17], s[4:5], 0, v[10:11]
	v_lshl_add_u64 v[10:11], s[10:11], 0, v[10:11]
	v_or_b32_e32 v18, 0xe50, v14
	global_load_dword v102, v[10:11], off
	v_lshlrev_b64 v[10:11], 2, v[18:19]
	global_load_dword v101, v[16:17], off
	v_lshl_add_u64 v[16:17], s[4:5], 0, v[10:11]
	v_lshl_add_u64 v[10:11], s[10:11], 0, v[10:11]
	v_or_b32_e32 v18, 0xe60, v14
	global_load_dword v104, v[10:11], off
	v_lshlrev_b64 v[10:11], 2, v[18:19]
	global_load_dword v103, v[16:17], off
	v_lshl_add_u64 v[16:17], s[4:5], 0, v[10:11]
	v_lshl_add_u64 v[10:11], s[10:11], 0, v[10:11]
	v_or_b32_e32 v18, 0xe70, v14
	global_load_dword v106, v[10:11], off
	v_lshlrev_b64 v[10:11], 2, v[18:19]
	v_lshl_add_u64 v[14:15], s[4:5], 0, v[10:11]
	v_lshl_add_u64 v[10:11], s[10:11], 0, v[10:11]
	global_load_dword v105, v[16:17], off
	global_load_dword v18, v[14:15], off
	s_nop 0
	global_load_dword v10, v[10:11], off
	s_waitcnt vmcnt(56)
	v_cvt_pk_f16_f32 v6, v112, v113
	v_cvt_pk_f16_f32 v7, v114, v115
	v_cvt_pk_f16_f32 v8, v116, v117
	v_cvt_pk_f16_f32 v9, v118, v119
	v_cvt_pk_f16_f32 v2, v37, v47
	v_cvt_pk_f16_f32 v3, v49, v51
	s_waitcnt vmcnt(52)
	v_cvt_pk_f16_f32 v4, v53, v55
	s_waitcnt vmcnt(49)
	v_cvt_pk_f16_f32 v5, v57, v59
	s_waitcnt vmcnt(45)
	v_cvt_pk_f16_f32 v14, v62, v64
	s_waitcnt vmcnt(41)
	v_cvt_pk_f16_f32 v15, v66, v68
	v_mfma_f32_16x16x32_f16 a[4:7], v[6:9], v[2:5], a[4:7]
	global_store_dwordx4 v108, v[6:9], s[26:27] offset:256
	v_cvt_pk_f16_f32 v2, v46, v48
	v_cvt_pk_f16_f32 v3, v50, v52
	v_cvt_pk_f16_f32 v4, v54, v56
	v_cvt_pk_f16_f32 v5, v58, v60
	s_waitcnt vmcnt(38)
	v_cvt_pk_f16_f32 v16, v70, v72
	s_waitcnt vmcnt(33)
	v_cvt_pk_f16_f32 v17, v74, v76
	v_mfma_f32_16x16x32_f16 a[0:3], v[6:9], v[2:5], a[0:3]
	v_cvt_pk_f16_f32 v2, v120, v121
	v_cvt_pk_f16_f32 v3, v122, v123
	v_cvt_pk_f16_f32 v4, v124, v125
	v_cvt_pk_f16_f32 v5, v126, v127
	v_cvt_pk_f16_f32 v6, v61, v63
	v_cvt_pk_f16_f32 v7, v65, v67
	v_cvt_pk_f16_f32 v8, v69, v71
	v_cvt_pk_f16_f32 v9, v73, v75
	v_mfma_f32_16x16x32_f16 a[0:3], v[2:5], v[14:17], a[0:3]
	global_store_dwordx4 v108, v[2:5], s[26:27] offset:320
	s_waitcnt vmcnt(31)
	v_cvt_pk_f16_f32 v14, v78, v80
	s_waitcnt vmcnt(27)
	v_cvt_pk_f16_f32 v15, v82, v84
	s_waitcnt vmcnt(23)
	v_cvt_pk_f16_f32 v16, v86, v88
	v_mfma_f32_16x16x32_f16 a[4:7], v[2:5], v[6:9], a[4:7]
	v_cvt_pk_f16_f32 v2, v128, v129
	v_cvt_pk_f16_f32 v3, v130, v131
	v_cvt_pk_f16_f32 v4, v132, v133
	v_cvt_pk_f16_f32 v5, v134, v135
	v_cvt_pk_f16_f32 v6, v77, v79
	v_cvt_pk_f16_f32 v7, v81, v83
	s_waitcnt vmcnt(22)
	v_cvt_pk_f16_f32 v8, v85, v87
	s_waitcnt vmcnt(19)
	v_cvt_pk_f16_f32 v9, v89, v91
	s_waitcnt vmcnt(18)
	v_cvt_pk_f16_f32 v17, v90, v92
	v_mfma_f32_16x16x32_f16 a[4:7], v[2:5], v[6:9], a[4:7]
	global_store_dwordx4 v108, v[2:5], s[26:27] offset:384
	s_waitcnt vmcnt(15)
	v_cvt_pk_f16_f32 v6, v93, v95
	s_waitcnt vmcnt(11)
	v_cvt_pk_f16_f32 v7, v97, v99
	s_waitcnt vmcnt(7)
	v_cvt_pk_f16_f32 v8, v101, v103
	v_mfma_f32_16x16x32_f16 a[0:3], v[2:5], v[14:17], a[0:3]
	v_cvt_pk_f16_f32 v2, v136, v137
	v_cvt_pk_f16_f32 v3, v138, v139
	v_cvt_pk_f16_f32 v4, v140, v141
	v_cvt_pk_f16_f32 v5, v142, v143
	v_cvt_pk_f16_f32 v14, v94, v96
	s_waitcnt vmcnt(4)
	v_cvt_pk_f16_f32 v9, v105, v18
	v_cvt_pk_f16_f32 v15, v98, v100
	v_cvt_pk_f16_f32 v16, v102, v104
	s_waitcnt vmcnt(3)
	v_cvt_pk_f16_f32 v17, v106, v10
	v_mfma_f32_16x16x32_f16 a[4:7], v[2:5], v[6:9], a[4:7]
	global_store_dwordx4 v108, v[2:5], s[26:27] offset:448
	s_nop 0
	v_mfma_f32_16x16x32_f16 a[0:3], v[2:5], v[14:17], a[0:3]
	v_lshlrev_b32_e32 v2, 11, v1
	v_lshlrev_b32_e32 v3, 2, v12
	v_lshlrev_b32_e32 v4, 8, v13
	v_lshlrev_b32_e32 v18, 2, v0
	s_movk_i32 s4, 0x3c0
	v_or3_b32 v2, v2, v3, v4
	v_and_or_b32 v10, v18, s4, v3
	ds_write_b32 v2, a4
	ds_write_b32 v2, a0 offset:1024
	ds_write_b32 v2, a5 offset:64
	ds_write_b32 v2, a1 offset:1088
	ds_write_b32 v2, a6 offset:128
	ds_write_b32 v2, a2 offset:1152
	ds_write_b32 v2, a7 offset:192
	ds_write_b32 v2, a3 offset:1216
	s_waitcnt lgkmcnt(0)
	s_barrier
	ds_read2st64_b32 v[2:3], v10 offset1:4
	ds_read2st64_b32 v[4:5], v10 offset0:8 offset1:12
	ds_read2st64_b32 v[6:7], v10 offset0:16 offset1:20
	ds_read2st64_b32 v[8:9], v10 offset0:24 offset1:28
	s_movk_i32 s4, 0x1000
	v_or_b32_e32 v20, 0x2000, v18
	s_waitcnt lgkmcnt(2)
	v_add_f32_e32 v2, v2, v4
	v_add_f32_e32 v3, v3, v5
	s_waitcnt lgkmcnt(1)
	v_add_f32_e32 v2, v2, v6
	v_add_f32_e32 v3, v3, v7
	v_lshl_add_u64 v[6:7], s[6:7], 0, v[18:19]
	s_waitcnt lgkmcnt(0)
	v_add_f32_e32 v2, v2, v8
	v_add_f32_e32 v3, v3, v9
	v_add_co_u32_e32 v4, vcc, s4, v6
	ds_write2st64_b32 v10, v2, v3 offset0:32 offset1:36
	v_or_b32_e32 v10, 0x1000, v18
	v_addc_co_u32_e32 v5, vcc, 0, v7, vcc
	s_waitcnt lgkmcnt(0)
	s_barrier
	global_load_dword v2, v18, s[6:7] offset:2048
	global_load_dword v3, v18, s[6:7] offset:3072
	global_load_dword v57, v10, s[6:7]
	global_load_dword v49, v[4:5], off offset:1024
	global_load_dword v50, v[4:5], off offset:2048
	global_load_dword v44, v[4:5], off offset:3072
	global_load_dword v51, v10, s[16:17]
	global_load_dword v13, v18, s[6:7]
	s_nop 0
	global_load_dword v5, v18, s[16:17]
	global_load_dword v10, v18, s[6:7] offset:1024
	global_load_dword v11, v18, s[16:17] offset:1024
	global_load_dword v4, v18, s[16:17] offset:2048
	global_load_dword v42, v18, s[8:9]
	global_load_dword v12, v18, s[16:17] offset:3072
	global_load_dword v40, v18, s[18:19]
	v_lshl_add_u64 v[8:9], s[16:17], 0, v[18:19]
	v_add_co_u32_e32 v14, vcc, s4, v8
	s_movk_i32 s4, 0x2000
	s_nop 0
	v_addc_co_u32_e32 v15, vcc, 0, v9, vcc
	v_add_co_u32_e32 v16, vcc, s4, v6
	s_mov_b32 s5, 0xc2000000
	s_nop 0
	v_addc_co_u32_e32 v17, vcc, 0, v7, vcc
	global_load_dword v56, v[14:15], off offset:1024
	global_load_dword v54, v[14:15], off offset:2048
	global_load_dword v52, v[14:15], off offset:3072
	global_load_dword v53, v20, s[6:7]
	global_load_dword v43, v[16:17], off offset:1024
	global_load_dword v30, v[16:17], off offset:2048
	global_load_dword v31, v[16:17], off offset:3072
	global_load_dword v45, v20, s[16:17]
	v_add_co_u32_e32 v14, vcc, s4, v8
	s_movk_i32 s4, 0x3000
	s_nop 0
	v_addc_co_u32_e32 v15, vcc, 0, v9, vcc
	v_add_co_u32_e32 v6, vcc, s4, v6
	v_or_b32_e32 v16, 0x3000, v18
	s_nop 0
	v_addc_co_u32_e32 v7, vcc, 0, v7, vcc
	global_load_dword v46, v[14:15], off offset:1024
	global_load_dword v34, v[14:15], off offset:2048
	global_load_dword v35, v[14:15], off offset:3072
	global_load_dword v32, v16, s[6:7]
	global_load_dword v33, v[6:7], off offset:1024
	global_load_dword v20, v[6:7], off offset:2048
	global_load_dword v21, v[6:7], off offset:3072
	global_load_dword v22, v16, s[16:17]
	v_add_co_u32_e32 v6, vcc, s4, v8
	s_and_b32 s4, s2, 0xffffff80
	s_nop 0
	v_addc_co_u32_e32 v7, vcc, 0, v9, vcc
	global_load_dword v23, v[6:7], off offset:1024
	global_load_dword v24, v[6:7], off offset:2048
	global_load_dword v25, v[6:7], off offset:3072
	v_lshl_or_b32 v6, v1, 5, s4
	s_lshr_b32 s4, s2, 2
	v_and_or_b32 v70, s4, 31, v6
	ds_read_b128 v[6:9], v19 offset:8192
	ds_read_b128 v[14:17], v19 offset:9216
	ds_read_b128 v[26:29], v19 offset:8208
	ds_read_b128 v[58:61], v19 offset:8224
	ds_read_b128 v[62:65], v19 offset:8240
	v_lshlrev_b32_e32 v18, 1, v36
	ds_read_b128 v[66:69], v19 offset:9232
	v_lshl_add_u64 v[72:73], s[24:25], 0, v[18:19]
	v_mov_b32_e32 v38, 0x42000000
	v_ashrrev_i32_e32 v71, 31, v70
	s_and_b32 s4, s22, 48
	s_lshl_b32 s22, s4, 7
	s_lshl_b32 s4, s4, 1
	s_waitcnt vmcnt(21) lgkmcnt(5)
	v_fma_f32 v18, v13, v6, v42
	v_fmac_f32_e32 v18, v10, v7
	s_waitcnt vmcnt(19) lgkmcnt(4)
	v_fma_f32 v37, v5, v14, v40
	v_fmac_f32_e32 v37, v11, v15
	v_fmac_f32_e32 v18, v2, v8
	v_fmac_f32_e32 v37, v4, v16
	v_fmac_f32_e32 v18, v3, v9
	v_fmac_f32_e32 v37, v12, v17
	ds_read_b128 v[6:9], v19 offset:9248
	s_waitcnt lgkmcnt(4)
	v_fmac_f32_e32 v18, v57, v26
	s_waitcnt lgkmcnt(1)
	v_fmac_f32_e32 v37, v51, v66
	v_fmac_f32_e32 v18, v49, v27
	s_waitcnt vmcnt(18)
	v_fmac_f32_e32 v37, v56, v67
	v_fmac_f32_e32 v18, v50, v28
	s_waitcnt vmcnt(17)
	v_fmac_f32_e32 v37, v54, v68
	v_fmac_f32_e32 v18, v44, v29
	s_waitcnt vmcnt(16)
	v_fmac_f32_e32 v37, v52, v69
	s_waitcnt vmcnt(15)
	v_fmac_f32_e32 v18, v53, v58
	s_waitcnt vmcnt(11) lgkmcnt(0)
	v_fmac_f32_e32 v37, v45, v6
	v_fmac_f32_e32 v18, v43, v59
	s_waitcnt vmcnt(10)
	v_fmac_f32_e32 v37, v46, v7
	v_pk_mul_f32 v[6:7], v[30:31], v[60:61]
	ds_read_b128 v[14:17], v19 offset:9264
	v_add_f32_e32 v6, v18, v6
	v_add_f32_e32 v18, v6, v7
	s_waitcnt vmcnt(8)
	v_pk_mul_f32 v[6:7], v[34:35], v[8:9]
	v_lshlrev_b64 v[26:27], 13, v[70:71]
	v_add_f32_e32 v6, v37, v6
	v_add_f32_e32 v8, v6, v7
	s_waitcnt vmcnt(6)
	v_pk_mul_f32 v[6:7], v[32:33], v[62:63]
	s_nop 0
	v_add_f32_e32 v6, v18, v6
	v_add_f32_e32 v9, v6, v7
	s_waitcnt vmcnt(2) lgkmcnt(0)
	v_pk_mul_f32 v[6:7], v[22:23], v[14:15]
	s_nop 0
	v_add_f32_e32 v6, v8, v6
	v_add_f32_e32 v8, v6, v7
	v_pk_mul_f32 v[6:7], v[20:21], v[64:65]
	s_nop 0
	v_add_f32_e32 v6, v9, v6
	v_add_f32_e32 v9, v6, v7
	s_waitcnt vmcnt(0)
	v_pk_mul_f32 v[6:7], v[24:25], v[16:17]
	s_nop 0
	v_add_f32_e32 v6, v8, v6
	v_add_f32_e32 v6, v6, v7
	v_med3_f32 v6, v6, s5, v38
	v_mul_f32_e32 v6, 0x3fb8aa3b, v6
	v_exp_f32_e32 v18, v6
	v_med3_f32 v6, v9, s5, v38
	v_mul_f32_e32 v6, 0x3fb8aa3b, v6
	v_exp_f32_e32 v37, v6
	v_lshl_add_u64 v[6:7], v[72:73], 0, v[26:27]
	v_cvt_pk_bf16_f32 v8, v18, s0
	v_lshl_add_u64 v[28:29], v[6:7], 0, s[22:23]
	global_store_short v[28:29], v8, off
	ds_read_b128 v[6:9], v19 offset:8256
	ds_read_b128 v[14:17], v19 offset:9280
	ds_read_b128 v[58:61], v19 offset:8272
	ds_read_b128 v[62:65], v19 offset:8288
	ds_read_b128 v[66:69], v19 offset:8304
	ds_read_b128 v[70:73], v19 offset:9296
	s_waitcnt lgkmcnt(5)
	v_fma_f32 v39, v13, v6, v42
	s_waitcnt lgkmcnt(4)
	v_fma_f32 v41, v5, v14, v40
	v_fmac_f32_e32 v39, v10, v7
	v_fmac_f32_e32 v41, v11, v15
	v_fmac_f32_e32 v39, v2, v8
	v_fmac_f32_e32 v41, v4, v16
	v_fmac_f32_e32 v39, v3, v9
	v_fmac_f32_e32 v41, v12, v17
	ds_read_b128 v[6:9], v19 offset:9312
	s_waitcnt lgkmcnt(4)
	v_fmac_f32_e32 v39, v57, v58
	s_waitcnt lgkmcnt(1)
	v_fmac_f32_e32 v41, v51, v70
	v_fmac_f32_e32 v39, v49, v59
	v_fmac_f32_e32 v41, v56, v71
	v_fmac_f32_e32 v39, v50, v60
	v_fmac_f32_e32 v41, v54, v72
	v_fmac_f32_e32 v39, v44, v61
	v_fmac_f32_e32 v41, v52, v73
	v_fmac_f32_e32 v39, v53, v62
	s_waitcnt lgkmcnt(0)
	v_fmac_f32_e32 v41, v45, v6
	v_fmac_f32_e32 v39, v43, v63
	v_fmac_f32_e32 v41, v46, v7
	v_pk_mul_f32 v[6:7], v[30:31], v[64:65]
	ds_read_b128 v[14:17], v19 offset:9328
	v_add_f32_e32 v6, v39, v6
	v_add_f32_e32 v39, v6, v7
	v_pk_mul_f32 v[6:7], v[34:35], v[8:9]
	s_nop 0
	v_add_f32_e32 v6, v41, v6
	v_add_f32_e32 v8, v6, v7
	v_pk_mul_f32 v[6:7], v[32:33], v[66:67]
	s_nop 0
	v_add_f32_e32 v6, v39, v6
	v_add_f32_e32 v9, v6, v7
	s_waitcnt lgkmcnt(0)
	v_pk_mul_f32 v[6:7], v[22:23], v[14:15]
	s_nop 0
	v_add_f32_e32 v6, v8, v6
	v_add_f32_e32 v8, v6, v7
	v_pk_mul_f32 v[6:7], v[20:21], v[68:69]
	s_nop 0
	v_add_f32_e32 v6, v9, v6
	v_add_f32_e32 v9, v6, v7
	v_pk_mul_f32 v[6:7], v[24:25], v[16:17]
	s_nop 0
	v_add_f32_e32 v6, v8, v6
	v_add_f32_e32 v6, v6, v7
	v_med3_f32 v6, v6, s5, v38
	v_mul_f32_e32 v6, 0x3fb8aa3b, v6
	v_med3_f32 v7, v9, s5, v38
	v_exp_f32_e32 v39, v6
	v_mul_f32_e32 v41, 0x3fb8aa3b, v7
	ds_read_b128 v[6:9], v19 offset:8320
	ds_read_b128 v[14:17], v19 offset:9344
	ds_read_b128 v[58:61], v19 offset:8336
	ds_read_b128 v[62:65], v19 offset:9360
	v_cvt_pk_bf16_f32 v47, v39, s0
	global_store_short v[28:29], v47, off offset:128
	s_waitcnt lgkmcnt(3)
	v_fma_f32 v47, v13, v6, v42
	s_waitcnt lgkmcnt(2)
	v_fma_f32 v48, v5, v14, v40
	v_fmac_f32_e32 v47, v10, v7
	v_fmac_f32_e32 v48, v11, v15
	v_fmac_f32_e32 v47, v2, v8
	v_fmac_f32_e32 v48, v4, v16
	v_fmac_f32_e32 v47, v3, v9
	v_fmac_f32_e32 v48, v12, v17
	s_waitcnt lgkmcnt(1)
	v_fmac_f32_e32 v47, v57, v58
	ds_read_b128 v[6:9], v19 offset:8352
	ds_read_b128 v[14:17], v19 offset:9376
	v_fmac_f32_e32 v47, v49, v59
	s_waitcnt lgkmcnt(2)
	v_fmac_f32_e32 v48, v51, v62
	v_fmac_f32_e32 v47, v50, v60
	v_fmac_f32_e32 v48, v56, v63
	v_fmac_f32_e32 v47, v44, v61
	v_fmac_f32_e32 v48, v54, v64
	ds_read_b128 v[58:61], v19 offset:8368
	s_waitcnt lgkmcnt(2)
	v_fmac_f32_e32 v47, v53, v6
	v_fmac_f32_e32 v48, v52, v65
	v_fmac_f32_e32 v47, v43, v7
	v_pk_mul_f32 v[6:7], v[30:31], v[8:9]
	ds_read_b128 v[62:65], v19 offset:9392
	s_waitcnt lgkmcnt(2)
	v_fmac_f32_e32 v48, v45, v14
	v_add_f32_e32 v6, v47, v6
	v_fmac_f32_e32 v48, v46, v15
	v_add_f32_e32 v8, v6, v7
	v_pk_mul_f32 v[6:7], v[34:35], v[16:17]
	v_exp_f32_e32 v41, v41
	v_add_f32_e32 v6, v48, v6
	v_add_f32_e32 v9, v6, v7
	s_waitcnt lgkmcnt(1)
	v_pk_mul_f32 v[6:7], v[32:33], v[58:59]
	s_nop 0
	v_add_f32_e32 v6, v8, v6
	v_add_f32_e32 v8, v6, v7
	s_waitcnt lgkmcnt(0)
	v_pk_mul_f32 v[6:7], v[22:23], v[62:63]
	s_nop 0
	v_add_f32_e32 v6, v9, v6
	v_add_f32_e32 v9, v6, v7
	v_pk_mul_f32 v[6:7], v[20:21], v[60:61]
	s_nop 0
	v_add_f32_e32 v6, v8, v6
	v_add_f32_e32 v8, v6, v7
	v_pk_mul_f32 v[6:7], v[24:25], v[64:65]
	s_nop 0
	v_add_f32_e32 v6, v9, v6
	v_add_f32_e32 v6, v6, v7
	v_med3_f32 v6, v6, s5, v38
	v_mul_f32_e32 v6, 0x3fb8aa3b, v6
	v_exp_f32_e32 v47, v6
	v_med3_f32 v6, v8, s5, v38
	v_mul_f32_e32 v6, 0x3fb8aa3b, v6
	v_exp_f32_e32 v48, v6
	v_cvt_pk_bf16_f32 v6, v47, s0
	global_store_short v[28:29], v6, off offset:256
	ds_read_b128 v[6:9], v19 offset:8384
	ds_read_b128 v[14:17], v19 offset:9408
	ds_read_b128 v[58:61], v19 offset:8400
	ds_read_b128 v[62:65], v19 offset:8416
	ds_read_b128 v[66:69], v19 offset:8432
	ds_read_b128 v[70:73], v19 offset:9424
	s_waitcnt lgkmcnt(5)
	v_fma_f32 v55, v13, v6, v42
	s_waitcnt lgkmcnt(4)
	v_fma_f32 v74, v5, v14, v40
	v_fmac_f32_e32 v55, v10, v7
	v_fmac_f32_e32 v74, v11, v15
	v_fmac_f32_e32 v55, v2, v8
	v_fmac_f32_e32 v74, v4, v16
	v_fmac_f32_e32 v55, v3, v9
	v_fmac_f32_e32 v74, v12, v17
	ds_read_b128 v[6:9], v19 offset:9440
	s_waitcnt lgkmcnt(4)
	v_fmac_f32_e32 v55, v57, v58
	s_waitcnt lgkmcnt(1)
	v_fmac_f32_e32 v74, v51, v70
	v_fmac_f32_e32 v55, v49, v59
	v_fmac_f32_e32 v74, v56, v71
	v_fmac_f32_e32 v55, v50, v60
	v_fmac_f32_e32 v74, v54, v72
	v_fmac_f32_e32 v55, v44, v61
	v_fmac_f32_e32 v74, v52, v73
	v_fmac_f32_e32 v55, v53, v62
	s_waitcnt lgkmcnt(0)
	v_fmac_f32_e32 v74, v45, v6
	v_fmac_f32_e32 v55, v43, v63
	v_fmac_f32_e32 v74, v46, v7
	v_pk_mul_f32 v[6:7], v[30:31], v[64:65]
	ds_read_b128 v[14:17], v19 offset:9456
	v_add_f32_e32 v6, v55, v6
	v_add_f32_e32 v55, v6, v7
	v_pk_mul_f32 v[6:7], v[34:35], v[8:9]
	s_nop 0
	v_add_f32_e32 v6, v74, v6
	v_add_f32_e32 v8, v6, v7
	v_pk_mul_f32 v[6:7], v[32:33], v[66:67]
	s_nop 0
	v_add_f32_e32 v6, v55, v6
	v_add_f32_e32 v9, v6, v7
	s_waitcnt lgkmcnt(0)
	v_pk_mul_f32 v[6:7], v[22:23], v[14:15]
	s_nop 0
	v_add_f32_e32 v6, v8, v6
	v_add_f32_e32 v8, v6, v7
	v_pk_mul_f32 v[6:7], v[20:21], v[68:69]
	s_nop 0
	v_add_f32_e32 v6, v9, v6
	v_add_f32_e32 v9, v6, v7
	v_pk_mul_f32 v[6:7], v[24:25], v[16:17]
	s_nop 0
	v_add_f32_e32 v6, v8, v6
	v_add_f32_e32 v6, v6, v7
	v_med3_f32 v6, v6, s5, v38
	v_mul_f32_e32 v6, 0x3fb8aa3b, v6
	v_med3_f32 v7, v9, s5, v38
	v_exp_f32_e32 v55, v6
	v_mul_f32_e32 v58, 0x3fb8aa3b, v7
	ds_read_b128 v[6:9], v19 offset:8448
	ds_read_b128 v[14:17], v19 offset:9472
	ds_read_b128 v[60:63], v19 offset:8464
	ds_read_b128 v[64:67], v19 offset:9488
	v_cvt_pk_bf16_f32 v59, v55, s0
	global_store_short v[28:29], v59, off offset:384
	s_waitcnt lgkmcnt(3)
	v_fma_f32 v59, v13, v6, v42
	s_waitcnt lgkmcnt(2)
	v_fma_f32 v68, v5, v14, v40
	v_fmac_f32_e32 v59, v10, v7
	v_fmac_f32_e32 v68, v11, v15
	v_fmac_f32_e32 v59, v2, v8
	v_fmac_f32_e32 v68, v4, v16
	v_fmac_f32_e32 v59, v3, v9
	v_fmac_f32_e32 v68, v12, v17
	s_waitcnt lgkmcnt(1)
	v_fmac_f32_e32 v59, v57, v60
	ds_read_b128 v[6:9], v19 offset:8480
	ds_read_b128 v[14:17], v19 offset:9504
	v_fmac_f32_e32 v59, v49, v61
	s_waitcnt lgkmcnt(2)
	v_fmac_f32_e32 v68, v51, v64
	v_fmac_f32_e32 v59, v50, v62
	v_fmac_f32_e32 v68, v56, v65
	v_fmac_f32_e32 v59, v44, v63
	v_fmac_f32_e32 v68, v54, v66
	ds_read_b128 v[60:63], v19 offset:8496
	s_waitcnt lgkmcnt(2)
	v_fmac_f32_e32 v59, v53, v6
	v_fmac_f32_e32 v68, v52, v67
	v_fmac_f32_e32 v59, v43, v7
	v_pk_mul_f32 v[6:7], v[30:31], v[8:9]
	ds_read_b128 v[64:67], v19 offset:9520
	s_waitcnt lgkmcnt(2)
	v_fmac_f32_e32 v68, v45, v14
	v_add_f32_e32 v6, v59, v6
	v_fmac_f32_e32 v68, v46, v15
	v_add_f32_e32 v8, v6, v7
	v_pk_mul_f32 v[6:7], v[34:35], v[16:17]
	v_exp_f32_e32 v58, v58
	v_add_f32_e32 v6, v68, v6
	v_add_f32_e32 v9, v6, v7
	s_waitcnt lgkmcnt(1)
	v_pk_mul_f32 v[6:7], v[32:33], v[60:61]
	s_nop 0
	v_add_f32_e32 v6, v8, v6
	v_add_f32_e32 v8, v6, v7
	s_waitcnt lgkmcnt(0)
	v_pk_mul_f32 v[6:7], v[22:23], v[64:65]
	s_nop 0
	v_add_f32_e32 v6, v9, v6
	v_add_f32_e32 v9, v6, v7
	v_pk_mul_f32 v[6:7], v[20:21], v[62:63]
	s_nop 0
	v_add_f32_e32 v6, v8, v6
	v_add_f32_e32 v8, v6, v7
	v_pk_mul_f32 v[6:7], v[24:25], v[66:67]
	s_nop 0
	v_add_f32_e32 v6, v9, v6
	v_add_f32_e32 v6, v6, v7
	v_med3_f32 v6, v6, s5, v38
	v_mul_f32_e32 v6, 0x3fb8aa3b, v6
	v_exp_f32_e32 v59, v6
	v_med3_f32 v6, v8, s5, v38
	v_mul_f32_e32 v6, 0x3fb8aa3b, v6
	v_exp_f32_e32 v60, v6
	v_cvt_pk_bf16_f32 v6, v59, s0
	global_store_short v[28:29], v6, off offset:512
	ds_read_b128 v[6:9], v19 offset:8512
	ds_read_b128 v[14:17], v19 offset:9536
	ds_read_b128 v[62:65], v19 offset:8528
	ds_read_b128 v[66:69], v19 offset:8544
	ds_read_b128 v[70:73], v19 offset:8560
	ds_read_b128 v[74:77], v19 offset:9552
	s_waitcnt lgkmcnt(5)
	v_fma_f32 v61, v13, v6, v42
	s_waitcnt lgkmcnt(4)
	v_fma_f32 v78, v5, v14, v40
	v_fmac_f32_e32 v61, v10, v7
	v_fmac_f32_e32 v78, v11, v15
	v_fmac_f32_e32 v61, v2, v8
	v_fmac_f32_e32 v78, v4, v16
	v_fmac_f32_e32 v61, v3, v9
	v_fmac_f32_e32 v78, v12, v17
	ds_read_b128 v[6:9], v19 offset:9568
	s_waitcnt lgkmcnt(4)
	v_fmac_f32_e32 v61, v57, v62
	s_waitcnt lgkmcnt(1)
	v_fmac_f32_e32 v78, v51, v74
	v_fmac_f32_e32 v61, v49, v63
	v_fmac_f32_e32 v78, v56, v75
	v_fmac_f32_e32 v61, v50, v64
	v_fmac_f32_e32 v78, v54, v76
	v_fmac_f32_e32 v61, v44, v65
	v_fmac_f32_e32 v78, v52, v77
	v_fmac_f32_e32 v61, v53, v66
	s_waitcnt lgkmcnt(0)
	v_fmac_f32_e32 v78, v45, v6
	v_fmac_f32_e32 v61, v43, v67
	v_fmac_f32_e32 v78, v46, v7
	v_pk_mul_f32 v[6:7], v[30:31], v[68:69]
	ds_read_b128 v[14:17], v19 offset:9584
	v_add_f32_e32 v6, v61, v6
	v_add_f32_e32 v61, v6, v7
	v_pk_mul_f32 v[6:7], v[34:35], v[8:9]
	s_nop 0
	v_add_f32_e32 v6, v78, v6
	v_add_f32_e32 v8, v6, v7
	v_pk_mul_f32 v[6:7], v[32:33], v[70:71]
	s_nop 0
	v_add_f32_e32 v6, v61, v6
	v_add_f32_e32 v9, v6, v7
	s_waitcnt lgkmcnt(0)
	v_pk_mul_f32 v[6:7], v[22:23], v[14:15]
	s_nop 0
	v_add_f32_e32 v6, v8, v6
	v_add_f32_e32 v8, v6, v7
	v_pk_mul_f32 v[6:7], v[20:21], v[72:73]
	s_nop 0
	v_add_f32_e32 v6, v9, v6
	v_add_f32_e32 v9, v6, v7
	v_pk_mul_f32 v[6:7], v[24:25], v[16:17]
	s_nop 0
	v_add_f32_e32 v6, v8, v6
	v_add_f32_e32 v6, v6, v7
	v_med3_f32 v6, v6, s5, v38
	v_mul_f32_e32 v6, 0x3fb8aa3b, v6
	v_med3_f32 v7, v9, s5, v38
	v_exp_f32_e32 v61, v6
	v_mul_f32_e32 v62, 0x3fb8aa3b, v7
	ds_read_b128 v[6:9], v19 offset:8576
	ds_read_b128 v[14:17], v19 offset:9600
	ds_read_b128 v[64:67], v19 offset:8592
	ds_read_b128 v[68:71], v19 offset:9616
	v_cvt_pk_bf16_f32 v63, v61, s0
	global_store_short v[28:29], v63, off offset:640
	s_waitcnt lgkmcnt(3)
	v_fma_f32 v63, v13, v6, v42
	s_waitcnt lgkmcnt(2)
	v_fma_f32 v72, v5, v14, v40
	v_fmac_f32_e32 v63, v10, v7
	v_fmac_f32_e32 v72, v11, v15
	v_fmac_f32_e32 v63, v2, v8
	v_fmac_f32_e32 v72, v4, v16
	v_fmac_f32_e32 v63, v3, v9
	v_fmac_f32_e32 v72, v12, v17
	s_waitcnt lgkmcnt(1)
	v_fmac_f32_e32 v63, v57, v64
	ds_read_b128 v[6:9], v19 offset:8608
	ds_read_b128 v[14:17], v19 offset:9632
	v_fmac_f32_e32 v63, v49, v65
	s_waitcnt lgkmcnt(2)
	v_fmac_f32_e32 v72, v51, v68
	v_fmac_f32_e32 v63, v50, v66
	v_fmac_f32_e32 v72, v56, v69
	v_fmac_f32_e32 v63, v44, v67
	v_fmac_f32_e32 v72, v54, v70
	ds_read_b128 v[64:67], v19 offset:8624
	s_waitcnt lgkmcnt(2)
	v_fmac_f32_e32 v63, v53, v6
	v_fmac_f32_e32 v72, v52, v71
	v_fmac_f32_e32 v63, v43, v7
	v_pk_mul_f32 v[6:7], v[30:31], v[8:9]
	ds_read_b128 v[68:71], v19 offset:9648
	s_waitcnt lgkmcnt(2)
	v_fmac_f32_e32 v72, v45, v14
	v_add_f32_e32 v6, v63, v6
	v_fmac_f32_e32 v72, v46, v15
	v_add_f32_e32 v8, v6, v7
	v_pk_mul_f32 v[6:7], v[34:35], v[16:17]
	v_exp_f32_e32 v62, v62
	v_add_f32_e32 v6, v72, v6
	v_add_f32_e32 v9, v6, v7
	s_waitcnt lgkmcnt(1)
	v_pk_mul_f32 v[6:7], v[32:33], v[64:65]
	s_nop 0
	v_add_f32_e32 v6, v8, v6
	v_add_f32_e32 v8, v6, v7
	s_waitcnt lgkmcnt(0)
	v_pk_mul_f32 v[6:7], v[22:23], v[68:69]
	s_nop 0
	v_add_f32_e32 v6, v9, v6
	v_add_f32_e32 v9, v6, v7
	v_pk_mul_f32 v[6:7], v[20:21], v[66:67]
	s_nop 0
	v_add_f32_e32 v6, v8, v6
	v_add_f32_e32 v8, v6, v7
	v_pk_mul_f32 v[6:7], v[24:25], v[70:71]
	s_nop 0
	v_add_f32_e32 v6, v9, v6
	v_add_f32_e32 v6, v6, v7
	v_med3_f32 v6, v6, s5, v38
	v_mul_f32_e32 v6, 0x3fb8aa3b, v6
	v_exp_f32_e32 v63, v6
	v_med3_f32 v6, v8, s5, v38
	v_mul_f32_e32 v6, 0x3fb8aa3b, v6
	v_exp_f32_e32 v64, v6
	v_cvt_pk_bf16_f32 v6, v63, s0
	global_store_short v[28:29], v6, off offset:768
	ds_read_b128 v[6:9], v19 offset:8640
	ds_read_b128 v[14:17], v19 offset:9664
	ds_read_b128 v[66:69], v19 offset:8656
	ds_read_b128 v[70:73], v19 offset:8672
	ds_read_b128 v[74:77], v19 offset:8688
	ds_read_b128 v[78:81], v19 offset:9680
	s_waitcnt lgkmcnt(5)
	v_fma_f32 v65, v13, v6, v42
	s_waitcnt lgkmcnt(4)
	v_fma_f32 v82, v5, v14, v40
	v_fmac_f32_e32 v65, v10, v7
	v_fmac_f32_e32 v82, v11, v15
	v_fmac_f32_e32 v65, v2, v8
	v_fmac_f32_e32 v82, v4, v16
	v_fmac_f32_e32 v65, v3, v9
	v_fmac_f32_e32 v82, v12, v17
	ds_read_b128 v[6:9], v19 offset:9696
	s_waitcnt lgkmcnt(4)
	v_fmac_f32_e32 v65, v57, v66
	s_waitcnt lgkmcnt(1)
	v_fmac_f32_e32 v82, v51, v78
	v_fmac_f32_e32 v65, v49, v67
	v_fmac_f32_e32 v82, v56, v79
	v_fmac_f32_e32 v65, v50, v68
	v_fmac_f32_e32 v82, v54, v80
	v_fmac_f32_e32 v65, v44, v69
	v_fmac_f32_e32 v82, v52, v81
	v_fmac_f32_e32 v65, v53, v70
	s_waitcnt lgkmcnt(0)
	v_fmac_f32_e32 v82, v45, v6
	v_fmac_f32_e32 v65, v43, v71
	v_fmac_f32_e32 v82, v46, v7
	v_pk_mul_f32 v[6:7], v[30:31], v[72:73]
	ds_read_b128 v[14:17], v19 offset:9712
	v_add_f32_e32 v6, v65, v6
	v_add_f32_e32 v65, v6, v7
	v_pk_mul_f32 v[6:7], v[34:35], v[8:9]
	s_nop 0
	v_add_f32_e32 v6, v82, v6
	v_add_f32_e32 v8, v6, v7
	v_pk_mul_f32 v[6:7], v[32:33], v[74:75]
	s_nop 0
	v_add_f32_e32 v6, v65, v6
	v_add_f32_e32 v9, v6, v7
	s_waitcnt lgkmcnt(0)
	v_pk_mul_f32 v[6:7], v[22:23], v[14:15]
	s_nop 0
	v_add_f32_e32 v6, v8, v6
	v_add_f32_e32 v8, v6, v7
	v_pk_mul_f32 v[6:7], v[20:21], v[76:77]
	s_nop 0
	v_add_f32_e32 v6, v9, v6
	v_add_f32_e32 v9, v6, v7
	v_pk_mul_f32 v[6:7], v[24:25], v[16:17]
	s_nop 0
	v_add_f32_e32 v6, v8, v6
	v_add_f32_e32 v6, v6, v7
	v_med3_f32 v6, v6, s5, v38
	v_mul_f32_e32 v6, 0x3fb8aa3b, v6
	v_exp_f32_e32 v65, v6
	v_med3_f32 v6, v9, s5, v38
	v_mul_f32_e32 v6, 0x3fb8aa3b, v6
	v_exp_f32_e32 v66, v6
	v_cvt_pk_bf16_f32 v6, v65, s0
	global_store_short v[28:29], v6, off offset:896
	ds_read_b128 v[6:9], v19 offset:8704
	ds_read_b128 v[14:17], v19 offset:9728
	ds_read_b128 v[68:71], v19 offset:8720
	ds_read_b128 v[72:75], v19 offset:8736
	ds_read_b128 v[76:79], v19 offset:8752
	ds_read_b128 v[80:83], v19 offset:9744
	s_waitcnt lgkmcnt(5)
	v_fma_f32 v67, v13, v6, v42
	s_waitcnt lgkmcnt(4)
	v_fma_f32 v84, v5, v14, v40
	v_fmac_f32_e32 v67, v10, v7
	v_fmac_f32_e32 v84, v11, v15
	v_fmac_f32_e32 v67, v2, v8
	v_fmac_f32_e32 v84, v4, v16
	v_fmac_f32_e32 v67, v3, v9
	v_fmac_f32_e32 v84, v12, v17
	ds_read_b128 v[6:9], v19 offset:9760
	s_waitcnt lgkmcnt(4)
	v_fmac_f32_e32 v67, v57, v68
	s_waitcnt lgkmcnt(1)
	v_fmac_f32_e32 v84, v51, v80
	v_fmac_f32_e32 v67, v49, v69
	v_fmac_f32_e32 v84, v56, v81
	v_fmac_f32_e32 v67, v50, v70
	v_fmac_f32_e32 v84, v54, v82
	v_fmac_f32_e32 v67, v44, v71
	v_fmac_f32_e32 v84, v52, v83
	v_fmac_f32_e32 v67, v53, v72
	s_waitcnt lgkmcnt(0)
	v_fmac_f32_e32 v84, v45, v6
	v_fmac_f32_e32 v67, v43, v73
	v_fmac_f32_e32 v84, v46, v7
	v_pk_mul_f32 v[6:7], v[30:31], v[74:75]
	ds_read_b128 v[14:17], v19 offset:9776
	v_add_f32_e32 v6, v67, v6
	v_add_f32_e32 v67, v6, v7
	v_pk_mul_f32 v[6:7], v[34:35], v[8:9]
	s_nop 0
	v_add_f32_e32 v6, v84, v6
	v_add_f32_e32 v8, v6, v7
	v_pk_mul_f32 v[6:7], v[32:33], v[76:77]
	s_nop 0
	v_add_f32_e32 v6, v67, v6
	v_add_f32_e32 v9, v6, v7
	s_waitcnt lgkmcnt(0)
	v_pk_mul_f32 v[6:7], v[22:23], v[14:15]
	s_nop 0
	v_add_f32_e32 v6, v8, v6
	v_add_f32_e32 v8, v6, v7
	v_pk_mul_f32 v[6:7], v[20:21], v[78:79]
	s_nop 0
	v_add_f32_e32 v6, v9, v6
	v_add_f32_e32 v9, v6, v7
	v_pk_mul_f32 v[6:7], v[24:25], v[16:17]
	s_nop 0
	v_add_f32_e32 v6, v8, v6
	v_add_f32_e32 v6, v6, v7
	v_med3_f32 v6, v6, s5, v38
	v_mul_f32_e32 v6, 0x3fb8aa3b, v6
	v_exp_f32_e32 v67, v6
	v_med3_f32 v6, v9, s5, v38
	v_mul_f32_e32 v6, 0x3fb8aa3b, v6
	v_exp_f32_e32 v68, v6
	v_cvt_pk_bf16_f32 v6, v67, s0
	global_store_short v[28:29], v6, off offset:1024
	ds_read_b128 v[6:9], v19 offset:8768
	ds_read_b128 v[14:17], v19 offset:9792
	ds_read_b128 v[70:73], v19 offset:8784
	ds_read_b128 v[74:77], v19 offset:8800
	ds_read_b128 v[78:81], v19 offset:8816
	ds_read_b128 v[82:85], v19 offset:9808
	s_waitcnt lgkmcnt(5)
	v_fma_f32 v69, v13, v6, v42
	s_waitcnt lgkmcnt(4)
	v_fma_f32 v86, v5, v14, v40
	v_fmac_f32_e32 v69, v10, v7
	v_fmac_f32_e32 v86, v11, v15
	v_fmac_f32_e32 v69, v2, v8
	v_fmac_f32_e32 v86, v4, v16
	v_fmac_f32_e32 v69, v3, v9
	v_fmac_f32_e32 v86, v12, v17
	ds_read_b128 v[6:9], v19 offset:9824
	s_waitcnt lgkmcnt(4)
	v_fmac_f32_e32 v69, v57, v70
	s_waitcnt lgkmcnt(1)
	v_fmac_f32_e32 v86, v51, v82
	v_fmac_f32_e32 v69, v49, v71
	v_fmac_f32_e32 v86, v56, v83
	v_fmac_f32_e32 v69, v50, v72
	v_fmac_f32_e32 v86, v54, v84
	v_fmac_f32_e32 v69, v44, v73
	v_fmac_f32_e32 v86, v52, v85
	v_fmac_f32_e32 v69, v53, v74
	s_waitcnt lgkmcnt(0)
	v_fmac_f32_e32 v86, v45, v6
	v_fmac_f32_e32 v69, v43, v75
	v_fmac_f32_e32 v86, v46, v7
	v_pk_mul_f32 v[6:7], v[30:31], v[76:77]
	ds_read_b128 v[14:17], v19 offset:9840
	v_add_f32_e32 v6, v69, v6
	v_add_f32_e32 v69, v6, v7
	v_pk_mul_f32 v[6:7], v[34:35], v[8:9]
	ds_read_b128 v[72:75], v19 offset:8848
	v_add_f32_e32 v6, v86, v6
	v_add_f32_e32 v8, v6, v7
	v_pk_mul_f32 v[6:7], v[32:33], v[78:79]
	ds_read_b128 v[76:79], v19 offset:9872
	v_add_f32_e32 v6, v69, v6
	v_add_f32_e32 v9, v6, v7
	s_waitcnt lgkmcnt(2)
	v_pk_mul_f32 v[6:7], v[22:23], v[14:15]
	s_nop 0
	v_add_f32_e32 v6, v8, v6
	v_add_f32_e32 v8, v6, v7
	v_pk_mul_f32 v[6:7], v[20:21], v[80:81]
	s_nop 0
	v_add_f32_e32 v6, v9, v6
	v_add_f32_e32 v9, v6, v7
	v_pk_mul_f32 v[6:7], v[24:25], v[16:17]
	ds_read_b128 v[14:17], v19 offset:9856
	v_add_f32_e32 v6, v8, v6
	v_add_f32_e32 v6, v6, v7
	v_med3_f32 v6, v6, s5, v38
	v_mul_f32_e32 v6, 0x3fb8aa3b, v6
	v_exp_f32_e32 v69, v6
	v_med3_f32 v6, v9, s5, v38
	v_mul_f32_e32 v6, 0x3fb8aa3b, v6
	v_exp_f32_e32 v70, v6
	ds_read_b128 v[6:9], v19 offset:8832
	v_cvt_pk_bf16_f32 v71, v69, s0
	global_store_short v[28:29], v71, off offset:1152
	s_waitcnt lgkmcnt(1)
	v_fma_f32 v80, v5, v14, v40
	v_fmac_f32_e32 v80, v11, v15
	s_waitcnt lgkmcnt(0)
	v_fma_f32 v71, v13, v6, v42
	v_fmac_f32_e32 v71, v10, v7
	v_fmac_f32_e32 v71, v2, v8
	v_fmac_f32_e32 v71, v3, v9
	v_fmac_f32_e32 v71, v57, v72
	v_fmac_f32_e32 v80, v4, v16
	v_fmac_f32_e32 v71, v49, v73
	v_fmac_f32_e32 v80, v12, v17
	ds_read_b128 v[6:9], v19 offset:8864
	ds_read_b128 v[14:17], v19 offset:8880
	v_fmac_f32_e32 v71, v50, v74
	v_fmac_f32_e32 v71, v44, v75
	ds_read_b128 v[72:75], v19 offset:9888
	v_fmac_f32_e32 v80, v51, v76
	v_fmac_f32_e32 v80, v56, v77
	v_fmac_f32_e32 v80, v54, v78
	s_waitcnt lgkmcnt(2)
	v_fmac_f32_e32 v71, v53, v6
	v_fmac_f32_e32 v80, v52, v79
	v_fmac_f32_e32 v71, v43, v7
	v_pk_mul_f32 v[6:7], v[30:31], v[8:9]
	ds_read_b128 v[76:79], v19 offset:9904
	s_waitcnt lgkmcnt(1)
	v_fmac_f32_e32 v80, v45, v72
	v_add_f32_e32 v6, v71, v6
	v_fmac_f32_e32 v80, v46, v73
	v_add_f32_e32 v8, v6, v7
	v_pk_mul_f32 v[6:7], v[34:35], v[74:75]
	s_nop 0
	v_add_f32_e32 v6, v80, v6
	v_add_f32_e32 v9, v6, v7
	v_pk_mul_f32 v[6:7], v[32:33], v[14:15]
	s_nop 0
	v_add_f32_e32 v6, v8, v6
	v_add_f32_e32 v8, v6, v7
	s_waitcnt lgkmcnt(0)
	v_pk_mul_f32 v[6:7], v[22:23], v[76:77]
	ds_read_b128 v[74:77], v19 offset:8912
	v_add_f32_e32 v6, v9, v6
	v_add_f32_e32 v9, v6, v7
	v_pk_mul_f32 v[6:7], v[20:21], v[16:17]
	ds_read_b128 v[14:17], v19 offset:9920
	v_add_f32_e32 v6, v8, v6
	v_add_f32_e32 v8, v6, v7
	v_pk_mul_f32 v[6:7], v[24:25], v[78:79]
	ds_read_b128 v[78:81], v19 offset:9936
	v_add_f32_e32 v6, v9, v6
	v_add_f32_e32 v6, v6, v7
	v_med3_f32 v6, v6, s5, v38
	v_mul_f32_e32 v6, 0x3fb8aa3b, v6
	v_exp_f32_e32 v71, v6
	v_med3_f32 v6, v8, s5, v38
	v_mul_f32_e32 v6, 0x3fb8aa3b, v6
	v_exp_f32_e32 v72, v6
	ds_read_b128 v[6:9], v19 offset:8896
	v_cvt_pk_bf16_f32 v73, v71, s0
	global_store_short v[28:29], v73, off offset:1280
	s_waitcnt lgkmcnt(2)
	v_fma_f32 v82, v5, v14, v40
	v_fmac_f32_e32 v82, v11, v15
	s_waitcnt lgkmcnt(0)
	v_fma_f32 v73, v13, v6, v42
	v_fmac_f32_e32 v73, v10, v7
	v_fmac_f32_e32 v73, v2, v8
	v_fmac_f32_e32 v73, v3, v9
	v_fmac_f32_e32 v73, v57, v74
	v_fmac_f32_e32 v82, v4, v16
	v_fmac_f32_e32 v73, v49, v75
	v_fmac_f32_e32 v82, v12, v17
	ds_read_b128 v[6:9], v19 offset:8928
	ds_read_b128 v[14:17], v19 offset:8944
	v_fmac_f32_e32 v73, v50, v76
	v_fmac_f32_e32 v73, v44, v77
	ds_read_b128 v[74:77], v19 offset:9952
	v_fmac_f32_e32 v82, v51, v78
	v_fmac_f32_e32 v82, v56, v79
	v_fmac_f32_e32 v82, v54, v80
	s_waitcnt lgkmcnt(2)
	v_fmac_f32_e32 v73, v53, v6
	v_fmac_f32_e32 v82, v52, v81
	v_fmac_f32_e32 v73, v43, v7
	v_pk_mul_f32 v[6:7], v[30:31], v[8:9]
	ds_read_b128 v[78:81], v19 offset:9968
	s_waitcnt lgkmcnt(1)
	v_fmac_f32_e32 v82, v45, v74
	v_add_f32_e32 v6, v73, v6
	v_fmac_f32_e32 v82, v46, v75
	v_add_f32_e32 v8, v6, v7
	v_pk_mul_f32 v[6:7], v[34:35], v[76:77]
	s_nop 0
	v_add_f32_e32 v6, v82, v6
	v_add_f32_e32 v9, v6, v7
	v_pk_mul_f32 v[6:7], v[32:33], v[14:15]
	s_nop 0
	v_add_f32_e32 v6, v8, v6
	v_add_f32_e32 v8, v6, v7
	s_waitcnt lgkmcnt(0)
	v_pk_mul_f32 v[6:7], v[22:23], v[78:79]
	s_nop 0
	v_add_f32_e32 v6, v9, v6
	v_add_f32_e32 v9, v6, v7
	v_pk_mul_f32 v[6:7], v[20:21], v[16:17]
	s_nop 0
	v_add_f32_e32 v6, v8, v6
	v_add_f32_e32 v8, v6, v7
	v_pk_mul_f32 v[6:7], v[24:25], v[80:81]
	s_nop 0
	v_add_f32_e32 v6, v9, v6
	v_add_f32_e32 v6, v6, v7
	v_med3_f32 v6, v6, s5, v38
	v_med3_f32 v7, v8, s5, v38
	v_mul_f32_e32 v6, 0x3fb8aa3b, v6
	v_mul_f32_e32 v7, 0x3fb8aa3b, v7
	v_exp_f32_e32 v73, v6
	v_exp_f32_e32 v74, v7
	ds_read_b128 v[6:9], v19 offset:8960
	ds_read_b128 v[14:17], v19 offset:9984
	ds_read_b128 v[76:79], v19 offset:8976
	v_cvt_pk_bf16_f32 v75, v73, s0
	global_store_short v[28:29], v75, off offset:1408
	s_waitcnt lgkmcnt(2)
	v_fma_f32 v75, v13, v6, v42
	v_fmac_f32_e32 v75, v10, v7
	ds_read_b128 v[80:83], v19 offset:10000
	v_fmac_f32_e32 v75, v2, v8
	s_waitcnt lgkmcnt(2)
	v_fma_f32 v84, v5, v14, v40
	v_fmac_f32_e32 v75, v3, v9
	v_fmac_f32_e32 v84, v11, v15
	ds_read_b128 v[6:9], v19 offset:8992
	s_waitcnt lgkmcnt(2)
	v_fmac_f32_e32 v75, v57, v76
	v_fmac_f32_e32 v84, v4, v16
	v_fmac_f32_e32 v75, v49, v77
	v_fmac_f32_e32 v84, v12, v17
	v_fmac_f32_e32 v75, v50, v78
	ds_read_b128 v[14:17], v19 offset:10016
	v_fmac_f32_e32 v75, v44, v79
	ds_read_b128 v[76:79], v19 offset:9008
	s_waitcnt lgkmcnt(3)
	v_fmac_f32_e32 v84, v51, v80
	v_fmac_f32_e32 v84, v56, v81
	v_fmac_f32_e32 v84, v54, v82
	s_waitcnt lgkmcnt(2)
	v_fmac_f32_e32 v75, v53, v6
	v_fmac_f32_e32 v84, v52, v83
	v_fmac_f32_e32 v75, v43, v7
	v_pk_mul_f32 v[6:7], v[30:31], v[8:9]
	ds_read_b128 v[80:83], v19 offset:10032
	s_waitcnt lgkmcnt(2)
	v_fmac_f32_e32 v84, v45, v14
	v_add_f32_e32 v6, v75, v6
	v_fmac_f32_e32 v84, v46, v15
	v_add_f32_e32 v8, v6, v7
	v_pk_mul_f32 v[6:7], v[34:35], v[16:17]
	s_nop 0
	v_add_f32_e32 v6, v84, v6
	v_add_f32_e32 v9, v6, v7
	s_waitcnt lgkmcnt(1)
	v_pk_mul_f32 v[6:7], v[32:33], v[76:77]
	s_nop 0
	v_add_f32_e32 v6, v8, v6
	v_add_f32_e32 v8, v6, v7
	s_waitcnt lgkmcnt(0)
	v_pk_mul_f32 v[6:7], v[22:23], v[80:81]
	s_nop 0
	v_add_f32_e32 v6, v9, v6
	v_add_f32_e32 v9, v6, v7
	v_pk_mul_f32 v[6:7], v[20:21], v[78:79]
	s_nop 0
	v_add_f32_e32 v6, v8, v6
	v_add_f32_e32 v8, v6, v7
	v_pk_mul_f32 v[6:7], v[24:25], v[82:83]
	s_nop 0
	v_add_f32_e32 v6, v9, v6
	v_add_f32_e32 v6, v6, v7
	v_med3_f32 v6, v6, s5, v38
	v_med3_f32 v7, v8, s5, v38
	v_mul_f32_e32 v6, 0x3fb8aa3b, v6
	v_mul_f32_e32 v7, 0x3fb8aa3b, v7
	v_exp_f32_e32 v75, v6
	v_exp_f32_e32 v76, v7
	ds_read_b128 v[6:9], v19 offset:9024
	ds_read_b128 v[14:17], v19 offset:10048
	ds_read_b128 v[78:81], v19 offset:9040
	v_cvt_pk_bf16_f32 v77, v75, s0
	global_store_short v[28:29], v77, off offset:1536
	s_waitcnt lgkmcnt(2)
	v_fma_f32 v77, v13, v6, v42
	v_fmac_f32_e32 v77, v10, v7
	ds_read_b128 v[82:85], v19 offset:10064
	v_fmac_f32_e32 v77, v2, v8
	s_waitcnt lgkmcnt(2)
	v_fma_f32 v86, v5, v14, v40
	v_fmac_f32_e32 v77, v3, v9
	v_fmac_f32_e32 v86, v11, v15
	ds_read_b128 v[6:9], v19 offset:9056
	s_waitcnt lgkmcnt(2)
	v_fmac_f32_e32 v77, v57, v78
	v_fmac_f32_e32 v86, v4, v16
	v_fmac_f32_e32 v77, v49, v79
	v_fmac_f32_e32 v86, v12, v17
	v_fmac_f32_e32 v77, v50, v80
	ds_read_b128 v[14:17], v19 offset:10080
	v_fmac_f32_e32 v77, v44, v81
	ds_read_b128 v[78:81], v19 offset:9072
	s_waitcnt lgkmcnt(3)
	v_fmac_f32_e32 v86, v51, v82
	v_fmac_f32_e32 v86, v56, v83
	v_fmac_f32_e32 v86, v54, v84
	s_waitcnt lgkmcnt(2)
	v_fmac_f32_e32 v77, v53, v6
	v_fmac_f32_e32 v86, v52, v85
	v_fmac_f32_e32 v77, v43, v7
	v_pk_mul_f32 v[6:7], v[30:31], v[8:9]
	ds_read_b128 v[82:85], v19 offset:10096
	s_waitcnt lgkmcnt(2)
	v_fmac_f32_e32 v86, v45, v14
	v_add_f32_e32 v6, v77, v6
	v_fmac_f32_e32 v86, v46, v15
	v_add_f32_e32 v8, v6, v7
	v_pk_mul_f32 v[6:7], v[34:35], v[16:17]
	s_nop 0
	v_add_f32_e32 v6, v86, v6
	v_add_f32_e32 v9, v6, v7
	s_waitcnt lgkmcnt(1)
	v_pk_mul_f32 v[6:7], v[32:33], v[78:79]
	s_nop 0
	v_add_f32_e32 v6, v8, v6
	v_add_f32_e32 v8, v6, v7
	s_waitcnt lgkmcnt(0)
	v_pk_mul_f32 v[6:7], v[22:23], v[82:83]
	s_nop 0
	v_add_f32_e32 v6, v9, v6
	v_add_f32_e32 v9, v6, v7
	v_pk_mul_f32 v[6:7], v[20:21], v[80:81]
	s_nop 0
	v_add_f32_e32 v6, v8, v6
	v_add_f32_e32 v8, v6, v7
	v_pk_mul_f32 v[6:7], v[24:25], v[84:85]
	s_nop 0
	v_add_f32_e32 v6, v9, v6
	v_add_f32_e32 v6, v6, v7
	v_med3_f32 v6, v6, s5, v38
	v_mul_f32_e32 v6, 0x3fb8aa3b, v6
	v_med3_f32 v7, v8, s5, v38
	v_exp_f32_e32 v77, v6
	v_mul_f32_e32 v6, 0x3fb8aa3b, v7
	v_exp_f32_e32 v78, v6
	ds_read_b128 v[6:9], v19 offset:9088
	v_cvt_pk_bf16_f32 v14, v77, s0
	global_store_short v[28:29], v14, off offset:1664
	ds_read_b128 v[14:17], v19 offset:9104
	ds_read_b128 v[80:83], v19 offset:10112
	s_waitcnt lgkmcnt(2)
	v_fma_f32 v79, v13, v6, v42
	v_fmac_f32_e32 v79, v10, v7
	v_fmac_f32_e32 v79, v2, v8
	v_fmac_f32_e32 v79, v3, v9
	ds_read_b128 v[6:9], v19 offset:10128
	s_waitcnt lgkmcnt(1)
	v_fma_f32 v86, v5, v80, v40
	v_fmac_f32_e32 v86, v11, v81
	v_fmac_f32_e32 v79, v57, v14
	v_fmac_f32_e32 v86, v4, v82
	v_fmac_f32_e32 v79, v49, v15
	v_fmac_f32_e32 v86, v12, v83
	v_fmac_f32_e32 v79, v50, v16
	v_fmac_f32_e32 v79, v44, v17
	ds_read_b128 v[14:17], v19 offset:9120
	s_waitcnt lgkmcnt(1)
	v_fmac_f32_e32 v86, v51, v6
	v_fmac_f32_e32 v86, v56, v7
	v_fmac_f32_e32 v86, v54, v8
	v_fmac_f32_e32 v86, v52, v9
	ds_read_b128 v[6:9], v19 offset:10144
	ds_read_b128 v[80:83], v19 offset:9136
	s_waitcnt lgkmcnt(2)
	v_fmac_f32_e32 v79, v53, v14
	v_fmac_f32_e32 v79, v43, v15
	v_pk_mul_f32 v[84:85], v[30:31], v[16:17]
	ds_read_b128 v[14:17], v19 offset:10160
	s_waitcnt lgkmcnt(2)
	v_fmac_f32_e32 v86, v45, v6
	v_add_f32_e32 v6, v79, v84
	v_fmac_f32_e32 v86, v46, v7
	v_add_f32_e32 v79, v6, v85
	v_pk_mul_f32 v[6:7], v[34:35], v[8:9]
	s_nop 0
	v_add_f32_e32 v6, v86, v6
	v_add_f32_e32 v8, v6, v7
	s_waitcnt lgkmcnt(1)
	v_pk_mul_f32 v[6:7], v[32:33], v[80:81]
	ds_read_b128 v[86:89], v19 offset:10176
	v_add_f32_e32 v6, v79, v6
	v_add_f32_e32 v9, v6, v7
	s_waitcnt lgkmcnt(1)
	v_pk_mul_f32 v[6:7], v[22:23], v[14:15]
	s_waitcnt lgkmcnt(0)
	v_fmac_f32_e32 v40, v5, v86
	v_add_f32_e32 v6, v8, v6
	v_add_f32_e32 v8, v6, v7
	v_pk_mul_f32 v[6:7], v[20:21], v[82:83]
	ds_read_b128 v[82:85], v19 offset:9152
	v_add_f32_e32 v6, v9, v6
	v_add_f32_e32 v9, v6, v7
	v_pk_mul_f32 v[6:7], v[24:25], v[16:17]
	ds_read_b128 v[14:17], v19 offset:10192
	v_add_f32_e32 v6, v8, v6
	v_add_f32_e32 v6, v6, v7
	v_med3_f32 v6, v6, s5, v38
	v_mul_f32_e32 v6, 0x3fb8aa3b, v6
	v_exp_f32_e32 v79, v6
	v_med3_f32 v7, v9, s5, v38
	v_mul_f32_e32 v7, 0x3fb8aa3b, v7
	v_exp_f32_e32 v80, v7
	v_cvt_pk_bf16_f32 v6, v79, s0
	global_store_short v[28:29], v6, off offset:1792
	ds_read_b128 v[6:9], v19 offset:9168
	s_waitcnt lgkmcnt(2)
	v_fmac_f32_e32 v42, v13, v82
	v_fmac_f32_e32 v42, v10, v83
	v_fmac_f32_e32 v40, v11, v87
	v_fmac_f32_e32 v42, v2, v84
	v_fmac_f32_e32 v42, v3, v85
	v_fmac_f32_e32 v40, v4, v88
	v_fmac_f32_e32 v40, v12, v89
	ds_read_b128 v[10:13], v19 offset:9184
	ds_read_b128 v[2:5], v19 offset:9200
	s_waitcnt lgkmcnt(2)
	v_fmac_f32_e32 v42, v57, v6
	v_fmac_f32_e32 v42, v49, v7
	ds_read_b128 v[82:85], v19 offset:10208
	v_fmac_f32_e32 v40, v51, v14
	v_fmac_f32_e32 v42, v50, v8
	v_fmac_f32_e32 v40, v56, v15
	v_fmac_f32_e32 v42, v44, v9
	v_fmac_f32_e32 v40, v54, v16
	s_waitcnt lgkmcnt(2)
	v_fmac_f32_e32 v42, v53, v10
	ds_read_b128 v[6:9], v19 offset:10224
	v_fmac_f32_e32 v40, v52, v17
	v_fmac_f32_e32 v42, v43, v11
	v_pk_mul_f32 v[10:11], v[30:31], v[12:13]
	s_waitcnt lgkmcnt(1)
	v_fmac_f32_e32 v40, v45, v82
	v_add_f32_e32 v10, v42, v10
	v_fmac_f32_e32 v40, v46, v83
	v_add_f32_e32 v12, v10, v11
	v_pk_mul_f32 v[10:11], v[34:35], v[84:85]
	v_pk_mul_f32 v[2:3], v[32:33], v[2:3]
	v_add_f32_e32 v10, v40, v10
	v_add_f32_e32 v2, v12, v2
	v_add_f32_e32 v10, v10, v11
	v_add_f32_e32 v11, v2, v3
	s_waitcnt lgkmcnt(0)
	v_pk_mul_f32 v[2:3], v[22:23], v[6:7]
	s_nop 0
	v_add_f32_e32 v2, v10, v2
	v_add_f32_e32 v6, v2, v3
	v_pk_mul_f32 v[2:3], v[20:21], v[4:5]
	v_cvt_pk_bf16_f32 v5, v64, v66
	v_add_f32_e32 v2, v11, v2
	v_add_f32_e32 v4, v2, v3
	v_pk_mul_f32 v[2:3], v[24:25], v[8:9]
	s_nop 0
	v_add_f32_e32 v2, v6, v2
	v_add_f32_e32 v2, v2, v3
	v_med3_f32 v2, v2, s5, v38
	v_mul_f32_e32 v2, 0x3fb8aa3b, v2
	v_exp_f32_e32 v10, v2
	v_med3_f32 v2, v4, s5, v38
	v_mul_f32_e32 v2, 0x3fb8aa3b, v2
	v_exp_f32_e32 v11, v2
	v_cvt_pk_bf16_f32 v2, v10, s0
	global_store_short v[28:29], v2, off offset:1920
	v_lshlrev_b32_e32 v2, 7, v36
	v_or3_b32 v26, v2, s4, v26
	v_lshl_add_u64 v[6:7], s[12:13], 0, v[26:27]
	v_cvt_pk_bf16_f32 v2, v37, v41
	v_cvt_pk_bf16_f32 v3, v48, v58
	v_cvt_pk_bf16_f32 v4, v60, v62
	global_store_dwordx4 v[6:7], v[2:5], off
	v_lshl_add_u64 v[8:9], s[14:15], 0, v[26:27]
	s_mov_b64 s[4:5], 0
	v_cvt_pk_bf16_f32 v2, v68, v70
	v_cvt_pk_bf16_f32 v3, v72, v74
	v_cvt_pk_bf16_f32 v4, v76, v78
	v_cvt_pk_bf16_f32 v5, v80, v11
	global_store_dwordx4 v[6:7], v[2:5], off offset:16
	s_nop 1
	v_cvt_pk_bf16_f32 v2, v18, v39
	v_cvt_pk_bf16_f32 v3, v47, v55
	v_cvt_pk_bf16_f32 v4, v59, v61
	v_cvt_pk_bf16_f32 v5, v63, v65
	global_store_dwordx4 v[8:9], v[2:5], off
	s_nop 1
	v_cvt_pk_bf16_f32 v2, v67, v69
	v_cvt_pk_bf16_f32 v3, v71, v73
	v_cvt_pk_bf16_f32 v4, v75, v77
	v_cvt_pk_bf16_f32 v5, v79, v10
	global_store_dwordx4 v[8:9], v[2:5], off offset:16
.LBB13_5:
	s_andn2_b64 vcc, exec, s[4:5]
	s_cbranch_vccnz .LBB13_17
	s_load_dwordx4 s[4:7], s[0:1], 0x68
	s_add_i32 s14, s2, 0xffffff00
	s_lshr_b32 s15, s14, 8
	s_cmpk_lt_u32 s14, 0x100
	s_cbranch_scc1 .LBB13_11
	s_load_dwordx2 s[8:9], s[0:1], 0x18
	s_cmp_lt_i32 s15, 2
	s_cbranch_scc1 .LBB13_12
	s_cmp_eq_u32 s15, 2
	s_mov_b64 s[10:11], -1
	s_cbranch_scc0 .LBB13_10
	s_mov_b64 s[10:11], 0

amdhsa.kernels:
  - .agpr_count:     0
    .args:
      - .actual_access:  read_only
        .address_space:  global
        .offset:         0
        .size:           8
        .value_kind:     global_buffer
      - .actual_access:  read_only
        .address_space:  global
        .offset:         8
        .size:           8
        .value_kind:     global_buffer
      - .actual_access:  write_only
        .address_space:  global
        .offset:         16
        .size:           8
        .value_kind:     global_buffer
      - .offset:         24
        .size:           4
        .value_kind:     by_value
      - .offset:         28
        .size:           4
        .value_kind:     by_value
      - .offset:         32
        .size:           4
        .value_kind:     by_value
      - .offset:         36
        .size:           4
        .value_kind:     by_value
    .group_segment_fixed_size: 8256
    .kernarg_segment_align: 8
    .kernarg_segment_size: 40
    .language:       OpenCL C
    .language_version:
      - 2
      - 0
    .max_flat_workgroup_size: 256
    .name:           _Z14gemm_f32_naivePKfS0_Pfiiii
    .private_segment_fixed_size: 0
    .sgpr_count:     24
    .sgpr_spill_count: 0
    .symbol:         _Z14gemm_f32_naivePKfS0_Pfiiii.kd
    .uniform_work_group_size: 1
    .uses_dynamic_stack: false
    .vgpr_count:     76
    .vgpr_spill_count: 0
    .wavefront_size: 64
  - .agpr_count:     0
    .args:
      - .actual_access:  read_only
        .address_space:  global
        .offset:         0
        .size:           8
        .value_kind:     global_buffer
      - .actual_access:  write_only
        .address_space:  global
        .offset:         8
        .size:           8
        .value_kind:     global_buffer
      - .actual_access:  write_only
        .address_space:  global
        .offset:         16
        .size:           8
        .value_kind:     global_buffer
      - .actual_access:  write_only
        .address_space:  global
        .offset:         24
        .size:           8
        .value_kind:     global_buffer
      - .actual_access:  write_only
        .address_space:  global
        .offset:         32
        .size:           8
        .value_kind:     global_buffer
      - .actual_access:  write_only
        .address_space:  global
        .offset:         40
        .size:           8
        .value_kind:     global_buffer
      - .actual_access:  write_only
        .address_space:  global
        .offset:         48
        .size:           8
        .value_kind:     global_buffer
    .group_segment_fixed_size: 0
    .kernarg_segment_align: 8
    .kernarg_segment_size: 56
    .language:       OpenCL C
    .language_version:
      - 2
      - 0
    .max_flat_workgroup_size: 256
    .name:           _Z10post_naivePKfPtS1_S1_S1_S1_S1_
    .private_segment_fixed_size: 0
    .sgpr_count:     28
    .sgpr_spill_count: 0
    .symbol:         _Z10post_naivePKfPtS1_S1_S1_S1_S1_.kd
    .uniform_work_group_size: 1
    .uses_dynamic_stack: false
    .vgpr_count:     38
    .vgpr_spill_count: 0
    .wavefront_size: 64
  - .agpr_count:     0
    .args:
      - .actual_access:  read_only
        .address_space:  global
        .offset:         0
        .size:           8
        .value_kind:     global_buffer
      - .actual_access:  read_only
        .address_space:  global
        .offset:         8
        .size:           8
        .value_kind:     global_buffer
      - .actual_access:  read_only
        .address_space:  global
        .offset:         16
        .size:           8
        .value_kind:     global_buffer
      - .actual_access:  read_only
        .address_space:  global
        .offset:         24
        .size:           8
        .value_kind:     global_buffer
      - .actual_access:  read_only
        .address_space:  global
        .offset:         32
        .size:           8
        .value_kind:     global_buffer
      - .actual_access:  read_only
        .address_space:  global
        .offset:         40
        .size:           8
        .value_kind:     global_buffer
      - .actual_access:  read_only
        .address_space:  global
        .offset:         48
        .size:           8
        .value_kind:     global_buffer
      - .actual_access:  write_only
        .address_space:  global
        .offset:         56
        .size:           8
        .value_kind:     global_buffer
      - .actual_access:  write_only
        .address_space:  global
        .offset:         64
        .size:           8
        .value_kind:     global_buffer
      - .actual_access:  write_only
        .address_space:  global
        .offset:         72
        .size:           8
        .value_kind:     global_buffer
      - .actual_access:  write_only
        .address_space:  global
        .offset:         80
        .size:           8
        .value_kind:     global_buffer
    .group_segment_fixed_size: 1152
    .kernarg_segment_align: 8
    .kernarg_segment_size: 88
    .language:       OpenCL C
    .language_version:
      - 2
      - 0
    .max_flat_workgroup_size: 256
    .name:           _Z11gates_naivePKfS0_S0_S0_S0_S0_S0_PtS1_S1_S1_
    .private_segment_fixed_size: 0
    .sgpr_count:     32
    .sgpr_spill_count: 0
    .symbol:         _Z11gates_naivePKfS0_S0_S0_S0_S0_S0_PtS1_S1_S1_.kd
    .uniform_work_group_size: 1
    .uses_dynamic_stack: false
    .vgpr_count:     66
    .vgpr_spill_count: 0
    .wavefront_size: 64
  - .agpr_count:     0
    .args:
      - .actual_access:  read_only
        .address_space:  global
        .offset:         0
        .size:           8
        .value_kind:     global_buffer
      - .actual_access:  read_only
        .address_space:  global
        .offset:         8
        .size:           8
        .value_kind:     global_buffer
      - .actual_access:  read_only
        .address_space:  global
        .offset:         16
        .size:           8
        .value_kind:     global_buffer
      - .actual_access:  read_only
        .address_space:  global
        .offset:         24
        .size:           8
        .value_kind:     global_buffer
      - .actual_access:  read_only
        .address_space:  global
        .offset:         32
        .size:           8
        .value_kind:     global_buffer
      - .actual_access:  read_only
        .address_space:  global
        .offset:         40
        .size:           8
        .value_kind:     global_buffer
      - .actual_access:  read_only
        .address_space:  global
        .offset:         48
        .size:           8
        .value_kind:     global_buffer
      - .actual_access:  write_only
        .address_space:  global
        .offset:         56
        .size:           8
        .value_kind:     global_buffer
    .group_segment_fixed_size: 12560
    .kernarg_segment_align: 8
    .kernarg_segment_size: 64
    .language:       OpenCL C
    .language_version:
      - 2
      - 0
    .max_flat_workgroup_size: 256
    .name:           _Z10attn_naivePKtS0_S0_S0_S0_S0_PKfPf
    .private_segment_fixed_size: 0
    .sgpr_count:     33
    .sgpr_spill_count: 0
    .symbol:         _Z10attn_naivePKtS0_S0_S0_S0_S0_PKfPf.kd
    .uniform_work_group_size: 1
    .uses_dynamic_stack: false
    .vgpr_count:     82
    .vgpr_spill_count: 0
    .wavefront_size: 64
  - .agpr_count:     0
    .args:
      - .address_space:  global
        .offset:         0
        .size:           8
        .value_kind:     global_buffer
      - .address_space:  global
        .offset:         8
        .size:           8
        .value_kind:     global_buffer
      - .actual_access:  write_only
        .address_space:  global
        .offset:         16
        .size:           8
        .value_kind:     global_buffer
    .group_segment_fixed_size: 0
    .kernarg_segment_align: 8
    .kernarg_segment_size: 24
    .language:       OpenCL C
    .language_version:
      - 2
      - 0
    .max_flat_workgroup_size: 512
    .name:           _Z8gemm_outPKtS0_Pf
    .private_segment_fixed_size: 0
    .sgpr_count:     26
    .sgpr_spill_count: 0
    .symbol:         _Z8gemm_outPKtS0_Pf.kd
    .uniform_work_group_size: 1
    .uses_dynamic_stack: false
    .vgpr_count:     158
    .vgpr_spill_count: 0
    .wavefront_size: 64
  - .agpr_count:     0
    .args:
      - .address_space:  global
        .offset:         0
        .size:           8
        .value_kind:     global_buffer
      - .address_space:  global
        .offset:         8
        .size:           8
        .value_kind:     global_buffer
      - .actual_access:  write_only
        .address_space:  global
        .offset:         16
        .size:           8
        .value_kind:     global_buffer
    .group_segment_fixed_size: 0
    .kernarg_segment_align: 8
    .kernarg_segment_size: 24
    .language:       OpenCL C
    .language_version:
      - 2
      - 0
    .max_flat_workgroup_size: 512
    .name:           _Z9gemm_out2PKtS0_Pf
    .private_segment_fixed_size: 0
    .sgpr_count:     27
    .sgpr_spill_count: 0
    .symbol:         _Z9gemm_out2PKtS0_Pf.kd
    .uniform_work_group_size: 1
    .uses_dynamic_stack: false
    .vgpr_count:     146
    .vgpr_spill_count: 0
    .wavefront_size: 64
  - .agpr_count:     0
    .args:
      - .actual_access:  read_only
        .address_space:  global
        .offset:         0
        .size:           8
        .value_kind:     global_buffer
      - .actual_access:  write_only
        .address_space:  global
        .offset:         8
        .size:           8
        .value_kind:     global_buffer
    .group_segment_fixed_size: 0
    .kernarg_segment_align: 8
    .kernarg_segment_size: 16
    .language:       OpenCL C
    .language_version:
      - 2
      - 0
    .max_flat_workgroup_size: 256
    .name:           _Z6conv_xPKfPt
    .private_segment_fixed_size: 0
    .sgpr_count:     14
    .sgpr_spill_count: 0
    .symbol:         _Z6conv_xPKfPt.kd
    .uniform_work_group_size: 1
    .uses_dynamic_stack: false
    .vgpr_count:     12
    .vgpr_spill_count: 0
    .wavefront_size: 64
  - .agpr_count:     0
    .args:
      - .actual_access:  read_only
        .address_space:  global
        .offset:         0
        .size:           8
        .value_kind:     global_buffer
      - .actual_access:  read_only
        .address_space:  global
        .offset:         8
        .size:           8
        .value_kind:     global_buffer
      - .actual_access:  read_only
        .address_space:  global
        .offset:         16
        .size:           8
        .value_kind:     global_buffer
      - .actual_access:  read_only
        .address_space:  global
        .offset:         24
        .size:           8
        .value_kind:     global_buffer
      - .actual_access:  read_only
        .address_space:  global
        .offset:         32
        .size:           8
        .value_kind:     global_buffer
      - .actual_access:  write_only
        .address_space:  global
        .offset:         40
        .size:           8
        .value_kind:     global_buffer
      - .actual_access:  write_only
        .address_space:  global
        .offset:         48
        .size:           8
        .value_kind:     global_buffer
    .group_segment_fixed_size: 16640
    .kernarg_segment_align: 8
    .kernarg_segment_size: 56
    .language:       OpenCL C
    .language_version:
      - 2
      - 0
    .max_flat_workgroup_size: 256
    .name:           _Z7conv_wTPKfS0_S0_S0_S0_PtS1_
    .private_segment_fixed_size: 0
    .sgpr_count:     26
    .sgpr_spill_count: 0
    .symbol:         _Z7conv_wTPKfS0_S0_S0_S0_PtS1_.kd
    .uniform_work_group_size: 1
    .uses_dynamic_stack: false
    .vgpr_count:     51
    .vgpr_spill_count: 0
    .wavefront_size: 64
  - .agpr_count:     0
    .args:
      - .actual_access:  read_only
        .address_space:  global
        .offset:         0
        .size:           8
        .value_kind:     global_buffer
      - .actual_access:  read_only
        .address_space:  global
        .offset:         8
        .size:           8
        .value_kind:     global_buffer
      - .actual_access:  write_only
        .address_space:  global
        .offset:         16
        .size:           8
        .value_kind:     global_buffer
    .group_segment_fixed_size: 0
    .kernarg_segment_align: 8
    .kernarg_segment_size: 24
    .language:       OpenCL C
    .language_version:
      - 2
      - 0
    .max_flat_workgroup_size: 256
    .name:           _Z7conv_w1PKfS0_Pt
    .private_segment_fixed_size: 0
    .sgpr_count:     16
    .sgpr_spill_count: 0
    .symbol:         _Z7conv_w1PKfS0_Pt.kd
    .uniform_work_group_size: 1
    .uses_dynamic_stack: false
    .vgpr_count:     6
    .vgpr_spill_count: 0
    .wavefront_size: 64
  - .agpr_count:     8
    .args:
      - .actual_access:  read_only
        .address_space:  global
        .offset:         0
        .size:           8
        .value_kind:     global_buffer
      - .actual_access:  read_only
        .address_space:  global
        .offset:         8
        .size:           8
        .value_kind:     global_buffer
      - .actual_access:  read_only
        .address_space:  global
        .offset:         16
        .size:           8
        .value_kind:     global_buffer
      - .actual_access:  read_only
        .address_space:  global
        .offset:         24
        .size:           8
        .value_kind:     global_buffer
      - .actual_access:  read_only
        .address_space:  global
        .offset:         32
        .size:           8
        .value_kind:     global_buffer
      - .actual_access:  read_only
        .address_space:  global
        .offset:         40
        .size:           8
        .value_kind:     global_buffer
      - .actual_access:  write_only
        .address_space:  global
        .offset:         48
        .size:           8
        .value_kind:     global_buffer
      - .actual_access:  write_only
        .address_space:  global
        .offset:         56
        .size:           8
        .value_kind:     global_buffer
      - .actual_access:  write_only
        .address_space:  global
        .offset:         64
        .size:           8
        .value_kind:     global_buffer
    .group_segment_fixed_size: 10240
    .kernarg_segment_align: 8
    .kernarg_segment_size: 72
    .language:       OpenCL C
    .language_version:
      - 2
      - 0
    .max_flat_workgroup_size: 256
    .name:           _Z10gates_fastPKtS0_PKfS2_S2_S2_PtS3_S3_
    .private_segment_fixed_size: 0
    .sgpr_count:     24
    .sgpr_spill_count: 0
    .symbol:         _Z10gates_fastPKtS0_PKfS2_S2_S2_PtS3_S3_.kd
    .uniform_work_group_size: 1
    .uses_dynamic_stack: false
    .vgpr_count:     96
    .vgpr_spill_count: 0
    .wavefront_size: 64
  - .agpr_count:     4
    .args:
      - .actual_access:  read_only
        .address_space:  global
        .offset:         0
        .size:           8
        .value_kind:     global_buffer
      - .actual_access:  read_only
        .address_space:  global
        .offset:         8
        .size:           8
        .value_kind:     global_buffer
      - .actual_access:  read_only
        .address_space:  global
        .offset:         16
        .size:           8
        .value_kind:     global_buffer
      - .actual_access:  read_only
        .address_space:  global
        .offset:         24
        .size:           8
        .value_kind:     global_buffer
      - .actual_access:  write_only
        .address_space:  global
        .offset:         32
        .size:           8
        .value_kind:     global_buffer
      - .actual_access:  write_only
        .address_space:  global
        .offset:         40
        .size:           8
        .value_kind:     global_buffer
      - .actual_access:  write_only
        .address_space:  global
        .offset:         48
        .size:           8
        .value_kind:     global_buffer
    .group_segment_fixed_size: 0
    .kernarg_segment_align: 8
    .kernarg_segment_size: 56
    .language:       OpenCL C
    .language_version:
      - 2
      - 0
    .max_flat_workgroup_size: 256
    .name:           _Z10state_fastPKtS0_S0_S0_PtS1_Pf
    .private_segment_fixed_size: 0
    .sgpr_count:     20
    .sgpr_spill_count: 0
    .symbol:         _Z10state_fastPKtS0_S0_S0_PtS1_Pf.kd
    .uniform_work_group_size: 1
    .uses_dynamic_stack: false
    .vgpr_count:     184
    .vgpr_spill_count: 0
    .wavefront_size: 64
  - .agpr_count:     0
    .args:
      - .actual_access:  read_only
        .address_space:  global
        .offset:         0
        .size:           8
        .value_kind:     global_buffer
      - .actual_access:  read_only
        .address_space:  global
        .offset:         8
        .size:           8
        .value_kind:     global_buffer
      - .actual_access:  read_only
        .address_space:  global
        .offset:         16
        .size:           8
        .value_kind:     global_buffer
      - .actual_access:  write_only
        .address_space:  global
        .offset:         24
        .size:           8
        .value_kind:     global_buffer
      - .actual_access:  write_only
        .address_space:  global
        .offset:         32
        .size:           8
        .value_kind:     global_buffer
      - .actual_access:  write_only
        .address_space:  global
        .offset:         40
        .size:           8
        .value_kind:     global_buffer
    .group_segment_fixed_size: 0
    .kernarg_segment_align: 8
    .kernarg_segment_size: 48
    .language:       OpenCL C
    .language_version:
      - 2
      - 0
    .max_flat_workgroup_size: 256
    .name:           _Z11prefix_fastPKtS0_PKfPtS3_Pf
    .private_segment_fixed_size: 0
    .sgpr_count:     106
    .sgpr_spill_count: 41
    .symbol:         _Z11prefix_fastPKtS0_PKfPtS3_Pf.kd
    .uniform_work_group_size: 1
    .uses_dynamic_stack: false
    .vgpr_count:     205
    .vgpr_spill_count: 0
    .wavefront_size: 64
  - .agpr_count:     0
    .args:
      - .address_space:  global
        .offset:         0
        .size:           8
        .value_kind:     global_buffer
      - .address_space:  global
        .offset:         8
        .size:           8
        .value_kind:     global_buffer
      - .address_space:  global
        .offset:         16
        .size:           8
        .value_kind:     global_buffer
      - .actual_access:  read_only
        .address_space:  global
        .offset:         24
        .size:           8
        .value_kind:     global_buffer
      - .address_space:  global
        .offset:         32
        .size:           8
        .value_kind:     global_buffer
      - .address_space:  global
        .offset:         40
        .size:           8
        .value_kind:     global_buffer
      - .address_space:  global
        .offset:         48
        .size:           8
        .value_kind:     global_buffer
      - .address_space:  global
        .offset:         56
        .size:           8
        .value_kind:     global_buffer
      - .address_space:  global
        .offset:         64
        .size:           8
        .value_kind:     global_buffer
      - .address_space:  global
        .offset:         72
        .size:           8
        .value_kind:     global_buffer
      - .address_space:  global
        .offset:         80
        .size:           8
        .value_kind:     global_buffer
      - .actual_access:  write_only
        .address_space:  global
        .offset:         88
        .size:           8
        .value_kind:     global_buffer
    .group_segment_fixed_size: 0
    .kernarg_segment_align: 8
    .kernarg_segment_size: 96
    .language:       OpenCL C
    .language_version:
      - 2
      - 0
    .max_flat_workgroup_size: 512
    .name:           _Z9attn_fastPKtS0_S0_S0_S0_S0_S0_S0_S0_PKfS2_Pt
    .private_segment_fixed_size: 0
    .sgpr_count:     52
    .sgpr_spill_count: 0
    .symbol:         _Z9attn_fastPKtS0_S0_S0_S0_S0_S0_S0_S0_PKfS2_Pt.kd
    .uniform_work_group_size: 1
    .uses_dynamic_stack: false
    .vgpr_count:     224
    .vgpr_spill_count: 0
    .wavefront_size: 64
  - .agpr_count:     12
    .args:
      - .actual_access:  read_only
        .address_space:  global
        .offset:         0
        .size:           8
        .value_kind:     global_buffer
      - .actual_access:  read_only
        .address_space:  global
        .offset:         8
        .size:           8
        .value_kind:     global_buffer
      - .actual_access:  read_only
        .address_space:  global
        .offset:         16
        .size:           8
        .value_kind:     global_buffer
      - .actual_access:  read_only
        .address_space:  global
        .offset:         24
        .size:           8
        .value_kind:     global_buffer
      - .actual_access:  read_only
        .address_space:  global
        .offset:         32
        .size:           8
        .value_kind:     global_buffer
      - .actual_access:  read_only
        .address_space:  global
        .offset:         40
        .size:           8
        .value_kind:     global_buffer
      - .actual_access:  read_only
        .address_space:  global
        .offset:         48
        .size:           8
        .value_kind:     global_buffer
      - .actual_access:  read_only
        .address_space:  global
        .offset:         56
        .size:           8
        .value_kind:     global_buffer
      - .actual_access:  read_only
        .address_space:  global
        .offset:         64
        .size:           8
        .value_kind:     global_buffer
      - .actual_access:  read_only
        .address_space:  global
        .offset:         72
        .size:           8
        .value_kind:     global_buffer
      - .actual_access:  read_only
        .address_space:  global
        .offset:         80
        .size:           8
        .value_kind:     global_buffer
      - .actual_access:  read_only
        .address_space:  global
        .offset:         88
        .size:           8
        .value_kind:     global_buffer
      - .actual_access:  write_only
        .address_space:  global
        .offset:         96
        .size:           8
        .value_kind:     global_buffer
      - .actual_access:  write_only
        .address_space:  global
        .offset:         104
        .size:           8
        .value_kind:     global_buffer
      - .actual_access:  write_only
        .address_space:  global
        .offset:         112
        .size:           8
        .value_kind:     global_buffer
      - .actual_access:  write_only
        .address_space:  global
        .offset:         120
        .size:           8
        .value_kind:     global_buffer
      - .actual_access:  write_only
        .address_space:  global
        .offset:         128
        .size:           8
        .value_kind:     global_buffer
      - .actual_access:  write_only
        .address_space:  global
        .offset:         136
        .size:           8
        .value_kind:     global_buffer
    .group_segment_fixed_size: 16640
    .kernarg_segment_align: 8
    .kernarg_segment_size: 144
    .language:       OpenCL C
    .language_version:
      - 2
      - 0
    .max_flat_workgroup_size: 256
    .name:           _Z11prep_kernelPKfS0_S0_S0_S0_S0_S0_S0_S0_S0_S0_S0_PtS1_S1_S1_S1_S1_
    .private_segment_fixed_size: 0
    .sgpr_count:     34
    .sgpr_spill_count: 0
    .symbol:         _Z11prep_kernelPKfS0_S0_S0_S0_S0_S0_S0_S0_S0_S0_S0_PtS1_S1_S1_S1_S1_.kd
    .uniform_work_group_size: 1
    .uses_dynamic_stack: false
    .vgpr_count:     164
    .vgpr_spill_count: 0
    .wavefront_size: 64
  - .agpr_count:     0
    .args:
      - .address_space:  global
        .offset:         0
        .size:           8
        .value_kind:     global_buffer
      - .address_space:  global
        .offset:         8
        .size:           8
        .value_kind:     global_buffer
      - .offset:         16
        .size:           4
        .value_kind:     by_value
      - .offset:         20
        .size:           4
        .value_kind:     by_value
      - .offset:         24
        .size:           4
        .value_kind:     by_value
      - .offset:         28
        .size:           4
        .value_kind:     by_value
      - .address_space:  global
        .offset:         32
        .size:           8
        .value_kind:     global_buffer
    .group_segment_fixed_size: 0
    .kernarg_segment_align: 8
    .kernarg_segment_size: 40
    .language:       OpenCL C
    .language_version:
      - 2
      - 0
    .max_flat_workgroup_size: 1024
    .name:           _Z9dbg_cmp16PKtS0_iiffPf
    .private_segment_fixed_size: 0
    .sgpr_count:     18
    .sgpr_spill_count: 0
    .symbol:         _Z9dbg_cmp16PKtS0_iiffPf.kd
    .uniform_work_group_size: 1
    .uses_dynamic_stack: false
    .vgpr_count:     5
    .vgpr_spill_count: 0
    .wavefront_size: 64
  - .agpr_count:     0
    .args:
      - .address_space:  global
        .offset:         0
        .size:           8
        .value_kind:     global_buffer
      - .address_space:  global
        .offset:         8
        .size:           8
        .value_kind:     global_buffer
      - .offset:         16
        .size:           4
        .value_kind:     by_value
      - .offset:         20
        .size:           4
        .value_kind:     by_value
      - .offset:         24
        .size:           56
        .value_kind:     by_value
    .group_segment_fixed_size: 0
    .kernarg_segment_align: 8
    .kernarg_segment_size: 80
    .language:       OpenCL C
    .language_version:
      - 2
      - 0
    .max_flat_workgroup_size: 512
    .name:           _Z5gemm8ILi0EEvPKtS1_ii7EpiArgs
    .private_segment_fixed_size: 0
    .sgpr_count:     36
    .sgpr_spill_count: 0
    .symbol:         _Z5gemm8ILi0EEvPKtS1_ii7EpiArgs.kd
    .uniform_work_group_size: 1
    .uses_dynamic_stack: false
    .vgpr_count:     246
    .vgpr_spill_count: 0
    .wavefront_size: 64
  - .agpr_count:     0
    .args:
      - .address_space:  global
        .offset:         0
        .size:           8
        .value_kind:     global_buffer
      - .address_space:  global
        .offset:         8
        .size:           8
        .value_kind:     global_buffer
      - .address_space:  global
        .offset:         16
        .size:           8
        .value_kind:     global_buffer
      - .address_space:  global
        .offset:         24
        .size:           8
        .value_kind:     global_buffer
      - .actual_access:  write_only
        .address_space:  global
        .offset:         32
        .size:           8
        .value_kind:     global_buffer
      - .actual_access:  write_only
        .address_space:  global
        .offset:         40
        .size:           8
        .value_kind:     global_buffer
      - .actual_access:  write_only
        .address_space:  global
        .offset:         48
        .size:           8
        .value_kind:     global_buffer
    .group_segment_fixed_size: 81920
    .kernarg_segment_align: 8
    .kernarg_segment_size: 56
    .language:       OpenCL C
    .language_version:
      - 2
      - 0
    .max_flat_workgroup_size: 256
    .name:           _Z9scan_fastILb1EEvPKtS1_S1_S1_PtS2_Pf
    .private_segment_fixed_size: 0
    .sgpr_count:     62
    .sgpr_spill_count: 0
    .symbol:         _Z9scan_fastILb1EEvPKtS1_S1_S1_PtS2_Pf.kd
    .uniform_work_group_size: 1
    .uses_dynamic_stack: false
    .vgpr_count:     160
    .vgpr_spill_count: 0
    .wavefront_size: 64
